# stack26 plus the first P.V MFMA of every step issued right after the softmax tail packing (behind a counted lgkmcnt wait), in front of the SALU, CV store and remaining V reads
# speedup vs baseline: 1.0035x; 1.0035x over previous
; DI void finishSM(f32x16& p0, f32x16& p1, float alpha, float& l_reg, bf16x8& pa0, bf16x8& pa1, bf16x8& pa2, bf16x8& pa3) {
; #pragma unroll
;     for (int r = 0; r < 16; ++r) p1[r] = __builtin_amdgcn_exp2f(p1[r]);
;     float ps = 0;
; #pragma unroll
;     for (int r = 0; r < 16; ++r) ps += p0[r];
; #pragma unroll
;     for (int r = 0; r < 16; ++r) ps += p1[r];
;     { auto rr = __builtin_amdgcn_permlane32_swap(__float_as_uint(ps), __float_as_uint(ps), false, false); ps = __uint_as_float(rr[0]) + __uint_as_float(rr[1]); }
;     l_reg = l_reg * alpha + ps;
;     ...
;     AT_PK4(p0, 0, pa0); AT_PK4(p0, 8, pa1); AT_PK4(p1, 0, pa2); AT_PK4(p1, 8, pa3);
;     ...
; }
; DI void qkt(f32x16& p0, f32x16& p1, const char* Ks, const bf16x8* qr, const f32x16& negm, int r32, int hi) {
; #pragma unroll
;     for (int d0 = 0; d0 < 4; ++d0) { const int cb = (d0 * 16 + hi * 8) * 2;
;         const bf16x8 b0 = *reinterpret_cast<const bf16x8*>(Ks + AT_KSWZ(r32, cb));
;         const bf16x8 b1 = *reinterpret_cast<const bf16x8*>(Ks + AT_KSWZ(32 + r32, cb));
;         p0 = __builtin_amdgcn_mfma_f32_32x32x16_bf16(b0, qr[d0], d0 == 0 ? negm : p0, 0, 0, 0);
;         p1 = __builtin_amdgcn_mfma_f32_32x32x16_bf16(b1, qr[d0], d0 == 0 ? negm : p1, 0, 0, 0); }
; }
; template <int D0> DI void pv_one(f32x16& od, int vb, bf16x8 pa0, bf16x8 pa1, bf16x8 pa2, bf16x8 pa3) {
;     const s16x4 l0 = tr_read<v_rd_off(D0, 0, 0)>(vb), h0 = tr_read<v_rd_off(D0, 0, 1)>(vb), l1 = tr_read<v_rd_off(D0, 1, 0)>(vb), h1 = tr_read<v_rd_off(D0, 1, 1)>(vb);
;     const s16x4 l2 = tr_read<v_rd_off(D0, 2, 0)>(vb), h2 = tr_read<v_rd_off(D0, 2, 1)>(vb), l3 = tr_read<v_rd_off(D0, 3, 0)>(vb), h3 = tr_read<v_rd_off(D0, 3, 1)>(vb);
;     asm volatile("s_waitcnt lgkmcnt(0)" ::: "memory"); AT_SBAR();
;     ...
;     od = __builtin_amdgcn_mfma_f32_32x32x16_bf16(AT_PK(l0, h0), pa0, od, 0, 0, 0);
;     od = __builtin_amdgcn_mfma_f32_32x32x16_bf16(AT_PK(l1, h1), pa1, od, 0, 0, 0);
;     od = __builtin_amdgcn_mfma_f32_32x32x16_bf16(AT_PK(l2, h2), pa2, od, 0, 0, 0);
;     od = __builtin_amdgcn_mfma_f32_32x32x16_bf16(AT_PK(l3, h3), pa3, od, 0, 0, 0);
;     ...
; }
; DI void pv_all_sm(f32x16* o, int vb, bf16x8 pa0, bf16x8 pa1, bf16x8 pa2, bf16x8 pa3, f32x16& p0, f32x16& p1, float& m_ref, f32x16& negm, float& alpha) {
;     pv_one<0>(o[0], vb, pa0, pa1, pa2, pa3);
;     float pmax = p0[0];
; #pragma unroll
;     for (int r = 1; r < 16; ++r) pmax = fmaxf(pmax, p0[r]);
.LBB4_702:
	s_lshl_b32 s26, s66, 13
	s_add_i32 s26, s26, 0
	v_add_u32_e32 v72, s26, v205
	v_add_u32_e32 v112, s26, v206
	v_add_u32_e32 v180, s26, v207
	s_waitcnt lgkmcnt(1)
	v_mfma_f32_32x32x16_bf16 v[128:143], v[64:67], v[156:159], v[80:95]
	ds_read_b128 v[64:67], v72 offset:49152
	ds_read_b128 v[72:75], v72 offset:53248
	ds_read_b128 v[76:79], v112 offset:49152
	ds_read_b128 v[220:223], v112 offset:53248
	s_add_u32 s74, s46, s28
	s_addc_u32 s75, s47, s29
	s_add_u32 s78, s74, 0x23808000
	s_addc_u32 s79, s75, 0
	s_add_u32 s80, s74, 0x2380a000
	s_add_u32 s76, s46, s30
	s_addc_u32 s77, s47, s31
	s_add_u32 s82, s76, 0x21804000
	s_addc_u32 s83, s77, 0
	s_lshl_b32 s92, s64, 14
	s_add_i32 s92, s92, s94
	s_mov_b32 m0, s92
	s_lshl_b32 s96, s64, 13
	global_load_lds_dwordx4 v249, s[78:79]
	s_addk_i32 s92, 0x400
	s_mov_b32 m0, s92
	s_add_i32 s96, s96, s95
	global_load_lds_dwordx4 v250, s[78:79]
	s_nop 0
	s_mov_b32 m0, s96
	s_nop 0
	global_load_lds_dwordx4 v251, s[82:83]
	v_exp_f32_e32 v186, v97
	v_exp_f32_e32 v213, v98
	v_exp_f32_e32 v214, v99
	v_exp_f32_e32 v219, v100
	v_exp_f32_e32 v228, v101
	s_waitcnt lgkmcnt(4)
	v_mfma_f32_32x32x16_bf16 v[112:127], v[68:71], v[156:159], v[80:95]
	ds_read_b128 v[68:71], v180 offset:49152
	ds_read_b128 v[224:227], v180 offset:53248
	v_exp_f32_e32 v180, v96
	v_cvt_pk_bf16_f32 v96, v216, v218
	v_cvt_pk_bf16_f32 v97, v179, v217
	v_cvt_pk_bf16_f32 v98, v177, v215
	v_cvt_pk_bf16_f32 v99, v176, v178
	s_waitcnt lgkmcnt(4)
	v_mfma_f32_32x32x16_bf16 v[112:127], v[72:75], v[152:155], v[112:127]
	v_add_f32_e32 v75, 0, v216
	v_add_f32_e32 v75, v218, v75
	v_add_f32_e32 v75, v179, v75
	v_add_f32_e32 v75, v217, v75
	v_add_f32_e32 v75, v177, v75
	v_add_f32_e32 v75, v215, v75
	v_add_f32_e32 v75, v176, v75
	v_mfma_f32_32x32x16_bf16 v[128:143], v[64:67], v[152:155], v[128:143]
	v_add_f32_e32 v75, v178, v75
	v_add_f32_e32 v75, v173, v75
	v_add_f32_e32 v75, v175, v75
	v_add_f32_e32 v75, v171, v75
	v_add_f32_e32 v75, v174, v75
	v_add_f32_e32 v75, v169, v75
	v_add_f32_e32 v75, v172, v75
	s_waitcnt lgkmcnt(3)
	v_mfma_f32_32x32x16_bf16 v[128:143], v[76:79], v[148:151], v[128:143]
	v_add_f32_e32 v75, v168, v75
	v_add_f32_e32 v75, v170, v75
	v_add_f32_e32 v75, v180, v75
	v_add_f32_e32 v75, v186, v75
	v_exp_f32_e32 v64, v102
	v_exp_f32_e32 v65, v103
	v_exp_f32_e32 v66, v104
	s_waitcnt lgkmcnt(2)
	v_mfma_f32_32x32x16_bf16 v[112:127], v[220:223], v[148:151], v[112:127]
	v_exp_f32_e32 v67, v105
	v_exp_f32_e32 v105, v106
	v_exp_f32_e32 v106, v107
	v_exp_f32_e32 v107, v108
	v_exp_f32_e32 v72, v109
	v_exp_f32_e32 v73, v110
	v_exp_f32_e32 v74, v111
	s_waitcnt lgkmcnt(1)
	v_mfma_f32_32x32x16_bf16 v[128:143], v[68:71], v[144:147], v[128:143]
	v_add_f32_e32 v68, v213, v75
	v_add_f32_e32 v68, v214, v68
	v_add_f32_e32 v68, v219, v68
	v_add_f32_e32 v68, v228, v68
	v_add_f32_e32 v68, v64, v68
	v_add_f32_e32 v68, v65, v68
	v_add_f32_e32 v68, v66, v68
	v_add_f32_e32 v68, v67, v68
	s_waitcnt lgkmcnt(0)
	v_mfma_f32_32x32x16_bf16 v[112:127], v[224:227], v[144:147], v[112:127]
	v_cvt_pk_bf16_f32 v100, v180, v186
	v_cvt_pk_bf16_f32 v103, v64, v65
	v_cvt_pk_bf16_f32 v104, v66, v67
	s_lshl_b32 s67, s65, 14
	v_add_u32_e32 v186, s67, v253
	ds_read_b64_tr_b16 v[64:65], v186 offset:0
	ds_read_b64_tr_b16 v[66:67], v186 offset:0x100
	v_add_f32_e32 v68, v105, v68
	v_add_f32_e32 v68, v106, v68
	v_add_f32_e32 v68, v107, v68
	v_add_f32_e32 v68, v72, v68
	v_add_f32_e32 v68, v73, v68
	v_add_f32_e32 v183, v74, v68
	ds_read_b64_tr_b16 v[68:69], v186 offset:0x1000
	ds_read_b64_tr_b16 v[70:71], v186 offset:0x1100
	v_cvt_pk_bf16_f32 v108, v173, v175
	v_cvt_pk_bf16_f32 v109, v171, v174
	v_cvt_pk_bf16_f32 v110, v169, v172
	v_cvt_pk_bf16_f32 v111, v168, v170
	v_cvt_pk_bf16_f32 v101, v213, v214
	v_cvt_pk_bf16_f32 v102, v219, v228
	v_cvt_pk_bf16_f32 v105, v105, v106
	v_cvt_pk_bf16_f32 v106, v107, v72
	v_cvt_pk_bf16_f32 v107, v73, v74
	s_nop 0
	s_waitcnt lgkmcnt(2)
	v_mfma_f32_32x32x16_bf16 v[32:47], v[64:67], v[96:99], v[32:47]
	s_addc_u32 s81, s75, 0
	s_andn2_b64 vcc, exec, s[2:3]
	s_cbranch_vccnz .LBB4_704
	s_mov_b64 s[2:3], s[8:9]
	global_store_dwordx2 v189, v[184:185], s[2:3] nt
.LBB4_704:
	ds_read_b64_tr_b16 v[72:73], v186 offset:0x2000
	ds_read_b64_tr_b16 v[74:75], v186 offset:0x2100
	ds_read_b64_tr_b16 v[76:77], v186 offset:0x3000
	ds_read_b64_tr_b16 v[78:79], v186 offset:0x3100
	s_waitcnt lgkmcnt(0)
	v_max_f32_e32 v64, v128, v129
	v_max3_f32 v64, v64, v130, v131
	v_max3_f32 v64, v64, v132, v133
	v_max3_f32 v64, v64, v134, v135
	v_max3_f32 v64, v64, v136, v137
	v_mfma_f32_32x32x16_bf16 v[32:47], v[68:71], v[108:111], v[32:47]
	v_max3_f32 v64, v64, v138, v139
	v_max3_f32 v66, v64, v140, v141
	ds_read_b64_tr_b16 v[64:65], v186 offset:0x200
	v_max3_f32 v180, v66, v142, v143
	ds_read_b64_tr_b16 v[66:67], v186 offset:0x300
	ds_read_b64_tr_b16 v[68:69], v186 offset:0x1200
	ds_read_b64_tr_b16 v[70:71], v186 offset:0x1300
	v_mfma_f32_32x32x16_bf16 v[32:47], v[72:75], v[100:103], v[32:47]
	ds_read_b64_tr_b16 v[72:73], v186 offset:0x2200
	ds_read_b64_tr_b16 v[74:75], v186 offset:0x2300
	ds_read_b64_tr_b16 v[214:215], v186 offset:0x3200
	ds_read_b64_tr_b16 v[216:217], v186 offset:0x3300
	v_mfma_f32_32x32x16_bf16 v[32:47], v[76:79], v[104:107], v[32:47]
	s_waitcnt lgkmcnt(0)
	v_mfma_f32_32x32x16_bf16 v[48:63], v[64:67], v[96:99], v[48:63]
	v_max3_f32 v76, v180, v112, v113
	v_max3_f32 v64, v76, v114, v115
	ds_read_b64_tr_b16 v[66:67], v186 offset:0x400
	v_max3_f32 v64, v64, v116, v117
	v_max3_f32 v64, v64, v118, v119
	v_max3_f32 v64, v64, v120, v121
	v_max3_f32 v64, v64, v122, v123
	v_mfma_f32_32x32x16_bf16 v[48:63], v[68:71], v[108:111], v[48:63]
	ds_read_b64_tr_b16 v[68:69], v186 offset:0x500
	ds_read_b64_tr_b16 v[70:71], v186 offset:0x1400
	v_max3_f32 v64, v64, v124, v125
	v_max3_f32 v64, v64, v126, v127
	v_mov_b32_e32 v65, v64
	s_nop 1
	v_permlane32_swap_b32_e32 v64, v65
	v_mfma_f32_32x32x16_bf16 v[48:63], v[72:75], v[100:103], v[48:63]
	ds_read_b64_tr_b16 v[72:73], v186 offset:0x1500
	ds_read_b64_tr_b16 v[74:75], v186 offset:0x2400
	ds_read_b64_tr_b16 v[76:77], v186 offset:0x2500
	ds_read_b64_tr_b16 v[218:219], v186 offset:0x3400
	ds_read_b64_tr_b16 v[220:221], v186 offset:0x3500
	v_mfma_f32_32x32x16_bf16 v[48:63], v[214:217], v[104:107], v[48:63]
	s_waitcnt lgkmcnt(0)
	v_max_f32_e32 v64, v64, v65
	v_mfma_f32_32x32x16_bf16 v[16:31], v[66:69], v[96:99], v[16:31]
	v_cmp_ge_f32_e32 vcc, s25, v64
	s_cmp_eq_u64 vcc, exec
	v_mfma_f32_32x32x16_bf16 v[16:31], v[70:73], v[108:111], v[16:31]
	v_mfma_f32_32x32x16_bf16 v[16:31], v[74:77], v[100:103], v[16:31]
	v_mfma_f32_32x32x16_bf16 v[16:31], v[218:221], v[104:107], v[16:31]
	s_cbranch_scc0 .LBB4_737
	v_mov_b32_e32 v180, 1.0

; #define AT_SBAR() __builtin_amdgcn_sched_barrier(0)
; template <int OFF> DI s16x4 tr_read(int vb) { s16x4 r; asm volatile("ds_read_b64_tr_b16 %0, %1 offset:%2" : "=&v"(r) : "v"(vb), "i"(OFF) : "memory"); return r; }
; DI void finishSM(f32x16& p0, f32x16& p1, float alpha, float& l_reg, bf16x8& pa0, bf16x8& pa1, bf16x8& pa2, bf16x8& pa3) {
; #pragma unroll
;     for (int r = 0; r < 16; ++r) p1[r] = __builtin_amdgcn_exp2f(p1[r]);
;     float ps = 0;
; #pragma unroll
;     for (int r = 0; r < 16; ++r) ps += p0[r];
; #pragma unroll
;     for (int r = 0; r < 16; ++r) ps += p1[r];
;     { auto rr = __builtin_amdgcn_permlane32_swap(__float_as_uint(ps), __float_as_uint(ps), false, false); ps = __uint_as_float(rr[0]) + __uint_as_float(rr[1]); }
;     l_reg = l_reg * alpha + ps;
;     ...
;     AT_PK4(p0, 0, pa0); AT_PK4(p0, 8, pa1); AT_PK4(p1, 0, pa2); AT_PK4(p1, 8, pa3);
;     ...
; }
; DI void qkt(f32x16& p0, f32x16& p1, const char* Ks, const bf16x8* qr, const f32x16& negm, int r32, int hi) {
; #pragma unroll
;     for (int d0 = 0; d0 < 4; ++d0) { const int cb = (d0 * 16 + hi * 8) * 2;
;         const bf16x8 b0 = *reinterpret_cast<const bf16x8*>(Ks + AT_KSWZ(r32, cb));
;         const bf16x8 b1 = *reinterpret_cast<const bf16x8*>(Ks + AT_KSWZ(32 + r32, cb));
;         p0 = __builtin_amdgcn_mfma_f32_32x32x16_bf16(b0, qr[d0], d0 == 0 ? negm : p0, 0, 0, 0);
;         p1 = __builtin_amdgcn_mfma_f32_32x32x16_bf16(b1, qr[d0], d0 == 0 ? negm : p1, 0, 0, 0); }
; }
; template <int D0> DI void pv_one(f32x16& od, int vb, bf16x8 pa0, bf16x8 pa1, bf16x8 pa2, bf16x8 pa3) {
;     const s16x4 l0 = tr_read<v_rd_off(D0, 0, 0)>(vb), h0 = tr_read<v_rd_off(D0, 0, 1)>(vb), l1 = tr_read<v_rd_off(D0, 1, 0)>(vb), h1 = tr_read<v_rd_off(D0, 1, 1)>(vb);
;     const s16x4 l2 = tr_read<v_rd_off(D0, 2, 0)>(vb), h2 = tr_read<v_rd_off(D0, 2, 1)>(vb), l3 = tr_read<v_rd_off(D0, 3, 0)>(vb), h3 = tr_read<v_rd_off(D0, 3, 1)>(vb);
;     asm volatile("s_waitcnt lgkmcnt(0)" ::: "memory"); AT_SBAR();
;     ...
;     od = __builtin_amdgcn_mfma_f32_32x32x16_bf16(AT_PK(l0, h0), pa0, od, 0, 0, 0);
;     od = __builtin_amdgcn_mfma_f32_32x32x16_bf16(AT_PK(l1, h1), pa1, od, 0, 0, 0);
;     od = __builtin_amdgcn_mfma_f32_32x32x16_bf16(AT_PK(l2, h2), pa2, od, 0, 0, 0);
;     od = __builtin_amdgcn_mfma_f32_32x32x16_bf16(AT_PK(l3, h3), pa3, od, 0, 0, 0);
;     ...
; }
.LBB4_723:
	v_exp_f32_e32 v186, v128
	v_exp_f32_e32 v230, v129
	v_exp_f32_e32 v231, v130
	v_exp_f32_e32 v232, v131
	v_exp_f32_e32 v233, v132
	v_exp_f32_e32 v234, v133
	v_exp_f32_e32 v235, v134
	v_exp_f32_e32 v236, v135
	v_exp_f32_e32 v237, v136
	v_exp_f32_e32 v238, v137
	v_exp_f32_e32 v239, v138
	v_exp_f32_e32 v240, v139
	v_exp_f32_e32 v241, v140
	v_exp_f32_e32 v242, v141
	v_exp_f32_e32 v243, v142
	v_exp_f32_e32 v244, v143
	v_add_u32_e32 v101, s78, v205
	v_add_u32_e32 v102, s78, v206
	v_add_u32_e32 v103, s78, v207
	ds_read_b128 v[172:175], v101 offset:49152
	ds_read_b128 v[176:179], v101 offset:53248
	ds_read_b128 v[214:217], v102 offset:49152
	ds_read_b128 v[218:221], v102 offset:53248
	ds_read_b128 v[222:225], v103 offset:49152
	ds_read_b128 v[226:229], v103 offset:53248
	v_exp_f32_e32 v112, v112
	v_exp_f32_e32 v113, v113
	v_exp_f32_e32 v114, v114
	s_waitcnt lgkmcnt(7)
	v_mfma_f32_32x32x16_bf16 v[128:143], v[96:99], v[156:159], v[80:95]
	s_add_u32 s78, s74, 0x2380c000
	s_addc_u32 s79, s75, 0
	s_add_u32 s74, s74, 0x2380e000
	s_addc_u32 s75, s75, 0
	s_add_u32 s76, s76, 0x21806000
	s_addc_u32 s77, s77, 0
	s_lshl_b32 s92, s65, 14
	s_add_i32 s92, s92, s94
	s_mov_b32 m0, s92
	s_lshl_b32 s96, s65, 13
	global_load_lds_dwordx4 v249, s[78:79]
	s_addk_i32 s92, 0x400
	s_mov_b32 m0, s92
	s_add_i32 s96, s96, s95
	global_load_lds_dwordx4 v250, s[78:79]
	s_nop 0
	s_mov_b32 m0, s96
	s_nop 0
	global_load_lds_dwordx4 v251, s[76:77]
	s_nop 0
	v_exp_f32_e32 v115, v115
	v_exp_f32_e32 v116, v116
	v_exp_f32_e32 v117, v117
	v_exp_f32_e32 v118, v118
	v_exp_f32_e32 v119, v119
	s_waitcnt lgkmcnt(6)
	v_mfma_f32_32x32x16_bf16 v[96:111], v[168:171], v[156:159], v[80:95]
	v_exp_f32_e32 v168, v120
	v_add_f32_e32 v120, 0, v186
	v_add_f32_e32 v120, v230, v120
	v_add_f32_e32 v120, v231, v120
	v_add_f32_e32 v120, v232, v120
	v_add_f32_e32 v120, v233, v120
	v_add_f32_e32 v120, v234, v120
	v_add_f32_e32 v120, v235, v120
	v_add_f32_e32 v120, v236, v120
	v_add_f32_e32 v120, v237, v120
	v_add_f32_e32 v120, v238, v120
	s_waitcnt lgkmcnt(5)
	v_mfma_f32_32x32x16_bf16 v[128:143], v[172:175], v[152:155], v[128:143]
	v_add_f32_e32 v120, v239, v120
	v_add_f32_e32 v120, v240, v120
	v_add_f32_e32 v120, v241, v120
	v_add_f32_e32 v120, v242, v120
	v_add_f32_e32 v120, v243, v120
	v_add_f32_e32 v120, v244, v120
	v_add_f32_e32 v120, v112, v120
	s_waitcnt lgkmcnt(4)
	v_mfma_f32_32x32x16_bf16 v[96:111], v[176:179], v[152:155], v[96:111]
	v_add_f32_e32 v120, v113, v120
	v_add_f32_e32 v120, v114, v120
	v_add_f32_e32 v120, v115, v120
	v_add_f32_e32 v120, v116, v120
	v_exp_f32_e32 v169, v121
	v_add_f32_e32 v120, v117, v120
	v_exp_f32_e32 v170, v122
	s_waitcnt lgkmcnt(3)
	v_mfma_f32_32x32x16_bf16 v[128:143], v[214:217], v[148:151], v[128:143]
	v_add_f32_e32 v120, v118, v120
	v_exp_f32_e32 v171, v123
	v_add_f32_e32 v120, v119, v120
	v_exp_f32_e32 v172, v124
	v_add_f32_e32 v120, v168, v120
	v_exp_f32_e32 v173, v125
	v_add_f32_e32 v120, v169, v120
	s_waitcnt lgkmcnt(2)
	v_mfma_f32_32x32x16_bf16 v[96:111], v[218:221], v[148:151], v[96:111]
	v_exp_f32_e32 v174, v126
	v_add_f32_e32 v120, v170, v120
	v_exp_f32_e32 v175, v127
	v_add_f32_e32 v120, v171, v120
	v_add_f32_e32 v120, v172, v120
	v_add_f32_e32 v120, v173, v120
	v_add_f32_e32 v120, v174, v120
	s_waitcnt lgkmcnt(1)
	v_mfma_f32_32x32x16_bf16 v[128:143], v[222:225], v[144:147], v[128:143]
	v_add_f32_e32 v213, v175, v120
	v_cvt_pk_bf16_f32 v120, v186, v230
	v_cvt_pk_bf16_f32 v121, v231, v232
	v_cvt_pk_bf16_f32 v122, v233, v234
	v_cvt_pk_bf16_f32 v123, v235, v236
	v_cvt_pk_bf16_f32 v124, v237, v238
	s_waitcnt lgkmcnt(0)
	v_mfma_f32_32x32x16_bf16 v[96:111], v[226:229], v[144:147], v[96:111]
	v_lshl_add_u32 v215, s66, 14, v253
	ds_read_b64_tr_b16 v[216:217], v215 offset:0
	ds_read_b64_tr_b16 v[218:219], v215 offset:0x100
	ds_read_b64_tr_b16 v[220:221], v215 offset:0x1000
	ds_read_b64_tr_b16 v[222:223], v215 offset:0x1100
	v_cvt_pk_bf16_f32 v125, v239, v240
	v_cvt_pk_bf16_f32 v126, v241, v242
	v_cvt_pk_bf16_f32 v127, v243, v244
	v_cvt_pk_bf16_f32 v112, v112, v113
	v_cvt_pk_bf16_f32 v113, v114, v115
	v_cvt_pk_bf16_f32 v114, v116, v117
	v_cvt_pk_bf16_f32 v115, v118, v119
	v_cvt_pk_bf16_f32 v116, v168, v169
	v_cvt_pk_bf16_f32 v117, v170, v171
	v_cvt_pk_bf16_f32 v118, v172, v173
	v_cvt_pk_bf16_f32 v119, v174, v175
	s_nop 0
	s_waitcnt lgkmcnt(2)
	v_mfma_f32_32x32x16_bf16 v[32:47], v[216:219], v[120:123], v[32:47]
	s_and_b64 vcc, exec, s[2:3]
	s_cbranch_vccnz .LBB4_725
	s_mov_b64 s[2:3], s[8:9]
	global_store_dwordx2 v189, v[184:185], s[2:3] nt
; #define AT_SBAR() __builtin_amdgcn_sched_barrier(0)
; template <int OFF> DI s16x4 tr_read(int vb) { s16x4 r; asm volatile("ds_read_b64_tr_b16 %0, %1 offset:%2" : "=&v"(r) : "v"(vb), "i"(OFF) : "memory"); return r; }
; template <int D0> DI void pv_one(f32x16& od, int vb, bf16x8 pa0, bf16x8 pa1, bf16x8 pa2, bf16x8 pa3) {
;     const s16x4 l0 = tr_read<v_rd_off(D0, 0, 0)>(vb), h0 = tr_read<v_rd_off(D0, 0, 1)>(vb), l1 = tr_read<v_rd_off(D0, 1, 0)>(vb), h1 = tr_read<v_rd_off(D0, 1, 1)>(vb);
;     const s16x4 l2 = tr_read<v_rd_off(D0, 2, 0)>(vb), h2 = tr_read<v_rd_off(D0, 2, 1)>(vb), l3 = tr_read<v_rd_off(D0, 3, 0)>(vb), h3 = tr_read<v_rd_off(D0, 3, 1)>(vb);
;     asm volatile("s_waitcnt lgkmcnt(0)" ::: "memory"); AT_SBAR();
;     ...
;     od = __builtin_amdgcn_mfma_f32_32x32x16_bf16(AT_PK(l0, h0), pa0, od, 0, 0, 0);
;     od = __builtin_amdgcn_mfma_f32_32x32x16_bf16(AT_PK(l1, h1), pa1, od, 0, 0, 0);
;     od = __builtin_amdgcn_mfma_f32_32x32x16_bf16(AT_PK(l2, h2), pa2, od, 0, 0, 0);
;     od = __builtin_amdgcn_mfma_f32_32x32x16_bf16(AT_PK(l3, h3), pa3, od, 0, 0, 0);
;     ...
; }
; DI void pv_all_sm(f32x16* o, int vb, bf16x8 pa0, bf16x8 pa1, bf16x8 pa2, bf16x8 pa3, f32x16& p0, f32x16& p1, float& m_ref, f32x16& negm, float& alpha) {
;     pv_one<0>(o[0], vb, pa0, pa1, pa2, pa3);
;     float pmax = p0[0];
; #pragma unroll
;     for (int r = 1; r < 16; ++r) pmax = fmaxf(pmax, p0[r]);
;     pv_one<1>(o[1], vb, pa0, pa1, pa2, pa3);
; #pragma unroll
;     for (int r = 0; r < 16; ++r) pmax = fmaxf(pmax, p1[r]);
;     { auto rr = __builtin_amdgcn_permlane32_swap(__float_as_uint(pmax), __float_as_uint(pmax), false, false); pmax = fmaxf(__uint_as_float(rr[0]), __uint_as_float(rr[1])); }
;     pv_one<2>(o[2], vb, pa0, pa1, pa2, pa3);
;     alpha = 1.f;
;     if (__builtin_expect(!__all(pmax <= THRL), 0)) {
;         const float dl = fmaxf(pmax, 0.f); m_ref += dl; alpha = __builtin_amdgcn_exp2f(-dl);
; #pragma unroll
;         for (int r = 0; r < 16; ++r) { p0[r] -= dl; p1[r] -= dl; }
; #pragma unroll
;         for (int r = 0; r < 16; ++r) negm[r] = -m_ref;
;     }
;     pv_one<3>(o[3], vb, pa0, pa1, pa2, pa3);
; #pragma unroll
;     for (int r = 0; r < 16; ++r) p0[r] = __builtin_amdgcn_exp2f(p0[r]);
; }
.LBB4_725:
	ds_read_b64_tr_b16 v[224:225], v215 offset:0x2000
	ds_read_b64_tr_b16 v[226:227], v215 offset:0x2100
	ds_read_b64_tr_b16 v[228:229], v215 offset:0x3000
	ds_read_b64_tr_b16 v[230:231], v215 offset:0x3100
	s_waitcnt lgkmcnt(0)
	v_max_f32_e32 v186, v128, v129
	ds_read_b64_tr_b16 v[216:217], v215 offset:0x200
	ds_read_b64_tr_b16 v[218:219], v215 offset:0x300
	v_max3_f32 v186, v186, v130, v131
	v_max3_f32 v186, v186, v132, v133
	v_mfma_f32_32x32x16_bf16 v[32:47], v[220:223], v[124:127], v[32:47]
	ds_read_b64_tr_b16 v[220:221], v215 offset:0x1200
	ds_read_b64_tr_b16 v[222:223], v215 offset:0x1300
	v_max3_f32 v186, v186, v134, v135
	v_max3_f32 v186, v186, v136, v137
	v_max3_f32 v186, v186, v138, v139
	v_max3_f32 v186, v186, v140, v141
	v_max3_f32 v186, v186, v142, v143
	v_mfma_f32_32x32x16_bf16 v[32:47], v[224:227], v[112:115], v[32:47]
	ds_read_b64_tr_b16 v[224:225], v215 offset:0x2200
	ds_read_b64_tr_b16 v[226:227], v215 offset:0x2300
	ds_read_b64_tr_b16 v[232:233], v215 offset:0x3200
	ds_read_b64_tr_b16 v[234:235], v215 offset:0x3300
	v_mfma_f32_32x32x16_bf16 v[32:47], v[228:231], v[116:119], v[32:47]
	s_waitcnt lgkmcnt(0)
	v_mfma_f32_32x32x16_bf16 v[48:63], v[216:219], v[120:123], v[48:63]
	v_max3_f32 v186, v186, v96, v97
	v_max3_f32 v186, v186, v98, v99
	ds_read_b64_tr_b16 v[218:219], v215 offset:0x400
	v_max3_f32 v186, v186, v100, v101
	v_max3_f32 v186, v186, v102, v103
	v_max3_f32 v186, v186, v104, v105
	v_max3_f32 v186, v186, v106, v107
	v_mfma_f32_32x32x16_bf16 v[48:63], v[220:223], v[124:127], v[48:63]
	ds_read_b64_tr_b16 v[220:221], v215 offset:0x500
	ds_read_b64_tr_b16 v[222:223], v215 offset:0x1400
	v_max3_f32 v186, v186, v108, v109
	v_max3_f32 v186, v186, v110, v111
	v_mov_b32_e32 v216, v186
	s_nop 1
	v_permlane32_swap_b32_e32 v186, v216
	v_mfma_f32_32x32x16_bf16 v[48:63], v[224:227], v[112:115], v[48:63]
	ds_read_b64_tr_b16 v[224:225], v215 offset:0x1500
	ds_read_b64_tr_b16 v[226:227], v215 offset:0x2400
	ds_read_b64_tr_b16 v[228:229], v215 offset:0x2500
	ds_read_b64_tr_b16 v[236:237], v215 offset:0x3400
	ds_read_b64_tr_b16 v[238:239], v215 offset:0x3500
	v_mfma_f32_32x32x16_bf16 v[48:63], v[232:235], v[116:119], v[48:63]
	s_waitcnt lgkmcnt(0)
	v_max_f32_e32 v216, v186, v216
	v_mfma_f32_32x32x16_bf16 v[16:31], v[218:221], v[120:123], v[16:31]
	v_cmp_ge_f32_e32 vcc, s25, v216
	s_cmp_eq_u64 vcc, exec
	v_mov_b32_e32 v186, 1.0
	v_mfma_f32_32x32x16_bf16 v[16:31], v[222:225], v[124:127], v[16:31]
	v_mfma_f32_32x32x16_bf16 v[16:31], v[226:229], v[112:115], v[16:31]
	v_mfma_f32_32x32x16_bf16 v[16:31], v[236:239], v[116:119], v[16:31]
	s_cbranch_scc0 .LBB4_738

; DI void finishSM(f32x16& p0, f32x16& p1, float alpha, float& l_reg, bf16x8& pa0, bf16x8& pa1, bf16x8& pa2, bf16x8& pa3) {
; #pragma unroll
;     for (int r = 0; r < 16; ++r) p1[r] = __builtin_amdgcn_exp2f(p1[r]);
;     float ps = 0;
; #pragma unroll
;     for (int r = 0; r < 16; ++r) ps += p0[r];
; #pragma unroll
;     for (int r = 0; r < 16; ++r) ps += p1[r];
;     { auto rr = __builtin_amdgcn_permlane32_swap(__float_as_uint(ps), __float_as_uint(ps), false, false); ps = __uint_as_float(rr[0]) + __uint_as_float(rr[1]); }
;     l_reg = l_reg * alpha + ps;
;     ...
;     AT_PK4(p0, 0, pa0); AT_PK4(p0, 8, pa1); AT_PK4(p1, 0, pa2); AT_PK4(p1, 8, pa3);
;     ...
; }
; DI void qkt(f32x16& p0, f32x16& p1, const char* Ks, const bf16x8* qr, const f32x16& negm, int r32, int hi) {
; #pragma unroll
;     for (int d0 = 0; d0 < 4; ++d0) { const int cb = (d0 * 16 + hi * 8) * 2;
;         const bf16x8 b0 = *reinterpret_cast<const bf16x8*>(Ks + AT_KSWZ(r32, cb));
;         const bf16x8 b1 = *reinterpret_cast<const bf16x8*>(Ks + AT_KSWZ(32 + r32, cb));
;         p0 = __builtin_amdgcn_mfma_f32_32x32x16_bf16(b0, qr[d0], d0 == 0 ? negm : p0, 0, 0, 0);
;         p1 = __builtin_amdgcn_mfma_f32_32x32x16_bf16(b1, qr[d0], d0 == 0 ? negm : p1, 0, 0, 0); }
; }
; template <int D0> DI void pv_one(f32x16& od, int vb, bf16x8 pa0, bf16x8 pa1, bf16x8 pa2, bf16x8 pa3) {
;     const s16x4 l0 = tr_read<v_rd_off(D0, 0, 0)>(vb), h0 = tr_read<v_rd_off(D0, 0, 1)>(vb), l1 = tr_read<v_rd_off(D0, 1, 0)>(vb), h1 = tr_read<v_rd_off(D0, 1, 1)>(vb);
;     const s16x4 l2 = tr_read<v_rd_off(D0, 2, 0)>(vb), h2 = tr_read<v_rd_off(D0, 2, 1)>(vb), l3 = tr_read<v_rd_off(D0, 3, 0)>(vb), h3 = tr_read<v_rd_off(D0, 3, 1)>(vb);
;     asm volatile("s_waitcnt lgkmcnt(0)" ::: "memory"); AT_SBAR();
;     ...
;     od = __builtin_amdgcn_mfma_f32_32x32x16_bf16(AT_PK(l0, h0), pa0, od, 0, 0, 0);
;     od = __builtin_amdgcn_mfma_f32_32x32x16_bf16(AT_PK(l1, h1), pa1, od, 0, 0, 0);
;     od = __builtin_amdgcn_mfma_f32_32x32x16_bf16(AT_PK(l2, h2), pa2, od, 0, 0, 0);
;     od = __builtin_amdgcn_mfma_f32_32x32x16_bf16(AT_PK(l3, h3), pa3, od, 0, 0, 0);
;     ...
; }
; DI void pv_all_sm(f32x16* o, int vb, bf16x8 pa0, bf16x8 pa1, bf16x8 pa2, bf16x8 pa3, f32x16& p0, f32x16& p1, float& m_ref, f32x16& negm, float& alpha) {
;     pv_one<0>(o[0], vb, pa0, pa1, pa2, pa3);
;     float pmax = p0[0];
; #pragma unroll
;     for (int r = 1; r < 16; ++r) pmax = fmaxf(pmax, p0[r]);
.LBB4_775:
	s_lshl_b32 s20, s30, 13
	s_add_i32 s20, s20, 0
	v_add_u32_e32 v72, s20, v208
	v_add_u32_e32 v112, s20, v209
	v_add_u32_e32 v180, s20, v210
	s_waitcnt lgkmcnt(1)
	v_mfma_f32_32x32x16_bf16 v[128:143], v[64:67], v[156:159], v[80:95]
	ds_read_b128 v[64:67], v72 offset:49152
	ds_read_b128 v[72:75], v72 offset:53248
	ds_read_b128 v[76:79], v112 offset:49152
	ds_read_b128 v[224:227], v112 offset:53248
	s_add_u32 s34, s46, s16
	s_addc_u32 s35, s47, s17
	s_add_u32 s24, s34, 0x23808000
	s_addc_u32 s25, s35, 0
	s_add_u32 s66, s34, 0x2380a000
	s_add_u32 s37, s46, s18
	s_addc_u32 s64, s47, s19
	s_add_u32 s74, s37, 0x21884000
	s_addc_u32 s75, s64, 0
	s_lshl_b32 s92, s15, 14
	s_add_i32 s92, s92, s94
	s_mov_b32 m0, s92
	s_lshl_b32 s96, s15, 13
	global_load_lds_dwordx4 v249, s[24:25]
	s_addk_i32 s92, 0x400
	s_mov_b32 m0, s92
	s_add_i32 s96, s96, s95
	global_load_lds_dwordx4 v250, s[24:25]
	s_nop 0
	s_mov_b32 m0, s96
	s_nop 0
	global_load_lds_dwordx4 v251, s[74:75]
	v_exp_f32_e32 v182, v97
	v_exp_f32_e32 v217, v98
	v_exp_f32_e32 v218, v99
	v_exp_f32_e32 v223, v100
	v_exp_f32_e32 v232, v101
	s_waitcnt lgkmcnt(4)
	v_mfma_f32_32x32x16_bf16 v[112:127], v[68:71], v[156:159], v[80:95]
	ds_read_b128 v[68:71], v180 offset:49152
	ds_read_b128 v[228:231], v180 offset:53248
	v_exp_f32_e32 v180, v96
	v_cvt_pk_bf16_f32 v96, v220, v222
	v_cvt_pk_bf16_f32 v97, v179, v221
	v_cvt_pk_bf16_f32 v98, v177, v219
	v_cvt_pk_bf16_f32 v99, v176, v178
	s_waitcnt lgkmcnt(4)
	v_mfma_f32_32x32x16_bf16 v[112:127], v[72:75], v[152:155], v[112:127]
	v_add_f32_e32 v75, 0, v220
	v_add_f32_e32 v75, v222, v75
	v_add_f32_e32 v75, v179, v75
	v_add_f32_e32 v75, v221, v75
	v_add_f32_e32 v75, v177, v75
	v_add_f32_e32 v75, v219, v75
	v_add_f32_e32 v75, v176, v75
	v_mfma_f32_32x32x16_bf16 v[128:143], v[64:67], v[152:155], v[128:143]
	v_add_f32_e32 v75, v178, v75
	v_add_f32_e32 v75, v173, v75
	v_add_f32_e32 v75, v175, v75
	v_add_f32_e32 v75, v171, v75
	v_add_f32_e32 v75, v174, v75
	v_add_f32_e32 v75, v169, v75
	v_add_f32_e32 v75, v172, v75
	s_waitcnt lgkmcnt(3)
	v_mfma_f32_32x32x16_bf16 v[128:143], v[76:79], v[148:151], v[128:143]
	v_add_f32_e32 v75, v168, v75
	v_add_f32_e32 v75, v170, v75
	v_add_f32_e32 v75, v180, v75
	v_add_f32_e32 v75, v182, v75
	v_exp_f32_e32 v64, v102
	v_exp_f32_e32 v65, v103
	v_exp_f32_e32 v66, v104
	s_waitcnt lgkmcnt(2)
	v_mfma_f32_32x32x16_bf16 v[112:127], v[224:227], v[148:151], v[112:127]
	v_exp_f32_e32 v67, v105
	v_exp_f32_e32 v105, v106
	v_exp_f32_e32 v106, v107
	v_exp_f32_e32 v107, v108
	v_exp_f32_e32 v72, v109
	v_exp_f32_e32 v73, v110
	v_exp_f32_e32 v74, v111
	s_waitcnt lgkmcnt(1)
	v_mfma_f32_32x32x16_bf16 v[128:143], v[68:71], v[144:147], v[128:143]
	v_add_f32_e32 v68, v217, v75
	v_add_f32_e32 v68, v218, v68
	v_add_f32_e32 v68, v223, v68
	v_add_f32_e32 v68, v232, v68
	v_add_f32_e32 v68, v64, v68
	v_add_f32_e32 v68, v65, v68
	v_add_f32_e32 v68, v66, v68
	v_add_f32_e32 v68, v67, v68
	s_waitcnt lgkmcnt(0)
	v_mfma_f32_32x32x16_bf16 v[112:127], v[228:231], v[144:147], v[112:127]
	v_cvt_pk_bf16_f32 v100, v180, v182
	v_cvt_pk_bf16_f32 v103, v64, v65
	v_cvt_pk_bf16_f32 v104, v66, v67
	s_lshl_b32 s31, s29, 14
	v_add_u32_e32 v182, s31, v253
	ds_read_b64_tr_b16 v[64:65], v182 offset:0
	ds_read_b64_tr_b16 v[66:67], v182 offset:0x100
	v_add_f32_e32 v68, v105, v68
	v_add_f32_e32 v68, v106, v68
	v_add_f32_e32 v68, v107, v68
	v_add_f32_e32 v68, v72, v68
	v_add_f32_e32 v68, v73, v68
	v_add_f32_e32 v215, v74, v68
	ds_read_b64_tr_b16 v[68:69], v182 offset:0x1000
	ds_read_b64_tr_b16 v[70:71], v182 offset:0x1100
	v_cvt_pk_bf16_f32 v108, v173, v175
	v_cvt_pk_bf16_f32 v109, v171, v174
	v_cvt_pk_bf16_f32 v110, v169, v172
	v_cvt_pk_bf16_f32 v111, v168, v170
	v_cvt_pk_bf16_f32 v101, v217, v218
	v_cvt_pk_bf16_f32 v102, v223, v232
	v_cvt_pk_bf16_f32 v105, v105, v106
	v_cvt_pk_bf16_f32 v106, v107, v72
	v_cvt_pk_bf16_f32 v107, v73, v74
	s_nop 0
	s_waitcnt lgkmcnt(2)
	v_mfma_f32_32x32x16_bf16 v[48:63], v[64:67], v[96:99], v[48:63]
	s_addc_u32 s67, s35, 0
	s_andn2_b64 vcc, exec, s[2:3]
	s_cbranch_vccnz .LBB4_777
	s_mov_b64 s[2:3], s[8:9]
	global_store_dwordx2 v193, v[184:185], s[2:3] nt
.LBB4_777:
	ds_read_b64_tr_b16 v[72:73], v182 offset:0x2000
	ds_read_b64_tr_b16 v[74:75], v182 offset:0x2100
	ds_read_b64_tr_b16 v[76:77], v182 offset:0x3000
	ds_read_b64_tr_b16 v[78:79], v182 offset:0x3100
	s_waitcnt lgkmcnt(0)
	v_max_f32_e32 v64, v128, v129
	v_max3_f32 v64, v64, v130, v131
	v_max3_f32 v64, v64, v132, v133
	v_max3_f32 v64, v64, v134, v135
	v_max3_f32 v64, v64, v136, v137
	v_mfma_f32_32x32x16_bf16 v[48:63], v[68:71], v[108:111], v[48:63]
	v_max3_f32 v64, v64, v138, v139
	v_max3_f32 v66, v64, v140, v141
	ds_read_b64_tr_b16 v[64:65], v182 offset:0x200
	v_max3_f32 v180, v66, v142, v143
	ds_read_b64_tr_b16 v[66:67], v182 offset:0x300
	ds_read_b64_tr_b16 v[68:69], v182 offset:0x1200
	ds_read_b64_tr_b16 v[70:71], v182 offset:0x1300
	v_mfma_f32_32x32x16_bf16 v[48:63], v[72:75], v[100:103], v[48:63]
	ds_read_b64_tr_b16 v[72:73], v182 offset:0x2200
	ds_read_b64_tr_b16 v[74:75], v182 offset:0x2300
	ds_read_b64_tr_b16 v[218:219], v182 offset:0x3200
	ds_read_b64_tr_b16 v[220:221], v182 offset:0x3300
	v_mfma_f32_32x32x16_bf16 v[48:63], v[76:79], v[104:107], v[48:63]
	s_waitcnt lgkmcnt(0)
	v_mfma_f32_32x32x16_bf16 v[32:47], v[64:67], v[96:99], v[32:47]
	v_max3_f32 v76, v180, v112, v113
	v_max3_f32 v64, v76, v114, v115
	ds_read_b64_tr_b16 v[66:67], v182 offset:0x400
	v_max3_f32 v64, v64, v116, v117
	v_max3_f32 v64, v64, v118, v119
	v_max3_f32 v64, v64, v120, v121
	v_max3_f32 v64, v64, v122, v123
	v_mfma_f32_32x32x16_bf16 v[32:47], v[68:71], v[108:111], v[32:47]
	ds_read_b64_tr_b16 v[68:69], v182 offset:0x500
	ds_read_b64_tr_b16 v[70:71], v182 offset:0x1400
	v_max3_f32 v64, v64, v124, v125
	v_max3_f32 v64, v64, v126, v127
	v_mov_b32_e32 v65, v64
	s_nop 1
	v_permlane32_swap_b32_e32 v64, v65
	v_mfma_f32_32x32x16_bf16 v[32:47], v[72:75], v[100:103], v[32:47]
	ds_read_b64_tr_b16 v[72:73], v182 offset:0x1500
	ds_read_b64_tr_b16 v[74:75], v182 offset:0x2400
	ds_read_b64_tr_b16 v[76:77], v182 offset:0x2500
	ds_read_b64_tr_b16 v[222:223], v182 offset:0x3400
	ds_read_b64_tr_b16 v[224:225], v182 offset:0x3500
	v_mfma_f32_32x32x16_bf16 v[32:47], v[218:221], v[104:107], v[32:47]
	s_waitcnt lgkmcnt(0)
	v_max_f32_e32 v64, v64, v65
	v_mfma_f32_32x32x16_bf16 v[16:31], v[66:69], v[96:99], v[16:31]
	v_cmp_ge_f32_e32 vcc, s26, v64
	s_cmp_eq_u64 vcc, exec
	v_mfma_f32_32x32x16_bf16 v[16:31], v[70:73], v[108:111], v[16:31]
	v_mfma_f32_32x32x16_bf16 v[16:31], v[74:77], v[100:103], v[16:31]
	v_mfma_f32_32x32x16_bf16 v[16:31], v[222:225], v[104:107], v[16:31]
	s_cbranch_scc0 .LBB4_810
	v_mov_b32_e32 v180, 1.0

; #define AT_SBAR() __builtin_amdgcn_sched_barrier(0)
; template <int OFF> DI s16x4 tr_read(int vb) { s16x4 r; asm volatile("ds_read_b64_tr_b16 %0, %1 offset:%2" : "=&v"(r) : "v"(vb), "i"(OFF) : "memory"); return r; }
; DI void finishSM(f32x16& p0, f32x16& p1, float alpha, float& l_reg, bf16x8& pa0, bf16x8& pa1, bf16x8& pa2, bf16x8& pa3) {
; #pragma unroll
;     for (int r = 0; r < 16; ++r) p1[r] = __builtin_amdgcn_exp2f(p1[r]);
;     float ps = 0;
; #pragma unroll
;     for (int r = 0; r < 16; ++r) ps += p0[r];
; #pragma unroll
;     for (int r = 0; r < 16; ++r) ps += p1[r];
;     { auto rr = __builtin_amdgcn_permlane32_swap(__float_as_uint(ps), __float_as_uint(ps), false, false); ps = __uint_as_float(rr[0]) + __uint_as_float(rr[1]); }
;     l_reg = l_reg * alpha + ps;
;     ...
;     AT_PK4(p0, 0, pa0); AT_PK4(p0, 8, pa1); AT_PK4(p1, 0, pa2); AT_PK4(p1, 8, pa3);
;     ...
; }
; DI void qkt(f32x16& p0, f32x16& p1, const char* Ks, const bf16x8* qr, const f32x16& negm, int r32, int hi) {
; #pragma unroll
;     for (int d0 = 0; d0 < 4; ++d0) { const int cb = (d0 * 16 + hi * 8) * 2;
;         const bf16x8 b0 = *reinterpret_cast<const bf16x8*>(Ks + AT_KSWZ(r32, cb));
;         const bf16x8 b1 = *reinterpret_cast<const bf16x8*>(Ks + AT_KSWZ(32 + r32, cb));
;         p0 = __builtin_amdgcn_mfma_f32_32x32x16_bf16(b0, qr[d0], d0 == 0 ? negm : p0, 0, 0, 0);
;         p1 = __builtin_amdgcn_mfma_f32_32x32x16_bf16(b1, qr[d0], d0 == 0 ? negm : p1, 0, 0, 0); }
; }
; template <int D0> DI void pv_one(f32x16& od, int vb, bf16x8 pa0, bf16x8 pa1, bf16x8 pa2, bf16x8 pa3) {
;     const s16x4 l0 = tr_read<v_rd_off(D0, 0, 0)>(vb), h0 = tr_read<v_rd_off(D0, 0, 1)>(vb), l1 = tr_read<v_rd_off(D0, 1, 0)>(vb), h1 = tr_read<v_rd_off(D0, 1, 1)>(vb);
;     const s16x4 l2 = tr_read<v_rd_off(D0, 2, 0)>(vb), h2 = tr_read<v_rd_off(D0, 2, 1)>(vb), l3 = tr_read<v_rd_off(D0, 3, 0)>(vb), h3 = tr_read<v_rd_off(D0, 3, 1)>(vb);
;     asm volatile("s_waitcnt lgkmcnt(0)" ::: "memory"); AT_SBAR();
;     ...
;     od = __builtin_amdgcn_mfma_f32_32x32x16_bf16(AT_PK(l0, h0), pa0, od, 0, 0, 0);
;     od = __builtin_amdgcn_mfma_f32_32x32x16_bf16(AT_PK(l1, h1), pa1, od, 0, 0, 0);
;     od = __builtin_amdgcn_mfma_f32_32x32x16_bf16(AT_PK(l2, h2), pa2, od, 0, 0, 0);
;     od = __builtin_amdgcn_mfma_f32_32x32x16_bf16(AT_PK(l3, h3), pa3, od, 0, 0, 0);
;     ...
; }
.LBB4_796:
	v_exp_f32_e32 v182, v128
	v_exp_f32_e32 v234, v129
	v_exp_f32_e32 v235, v130
	v_exp_f32_e32 v236, v131
	v_exp_f32_e32 v237, v132
	v_exp_f32_e32 v238, v133
	v_exp_f32_e32 v239, v134
	v_exp_f32_e32 v240, v135
	v_exp_f32_e32 v241, v136
	v_exp_f32_e32 v242, v137
	v_exp_f32_e32 v243, v138
	v_exp_f32_e32 v244, v139
	v_exp_f32_e32 v245, v140
	v_exp_f32_e32 v246, v141
	v_exp_f32_e32 v247, v142
	v_exp_f32_e32 v248, v143
	v_add_u32_e32 v101, s65, v208
	v_add_u32_e32 v102, s65, v209
	v_add_u32_e32 v103, s65, v210
	ds_read_b128 v[172:175], v101 offset:49152
	ds_read_b128 v[176:179], v101 offset:53248
	ds_read_b128 v[218:221], v102 offset:49152
	ds_read_b128 v[222:225], v102 offset:53248
	ds_read_b128 v[226:229], v103 offset:49152
	ds_read_b128 v[230:233], v103 offset:53248
	v_exp_f32_e32 v112, v112
	v_exp_f32_e32 v113, v113
	v_exp_f32_e32 v114, v114
	s_waitcnt lgkmcnt(7)
	v_mfma_f32_32x32x16_bf16 v[128:143], v[96:99], v[156:159], v[80:95]
	s_add_u32 s24, s34, 0x2380c000
	s_addc_u32 s25, s35, 0
	s_add_u32 s34, s34, 0x2380e000
	s_addc_u32 s35, s35, 0
	s_add_u32 s66, s37, 0x21886000
	s_addc_u32 s67, s64, 0
	s_lshl_b32 s92, s29, 14
	s_add_i32 s92, s92, s94
	s_mov_b32 m0, s92
	s_lshl_b32 s96, s29, 13
	global_load_lds_dwordx4 v249, s[24:25]
	s_addk_i32 s92, 0x400
	s_mov_b32 m0, s92
	s_add_i32 s96, s96, s95
	global_load_lds_dwordx4 v250, s[24:25]
	s_nop 0
	s_mov_b32 m0, s96
	s_nop 0
	global_load_lds_dwordx4 v251, s[66:67]
	s_nop 0
	v_exp_f32_e32 v115, v115
	v_exp_f32_e32 v116, v116
	v_exp_f32_e32 v117, v117
	v_exp_f32_e32 v118, v118
	v_exp_f32_e32 v119, v119
	s_waitcnt lgkmcnt(6)
	v_mfma_f32_32x32x16_bf16 v[96:111], v[168:171], v[156:159], v[80:95]
	v_exp_f32_e32 v168, v120
	v_add_f32_e32 v120, 0, v182
	v_add_f32_e32 v120, v234, v120
	v_add_f32_e32 v120, v235, v120
	v_add_f32_e32 v120, v236, v120
	v_add_f32_e32 v120, v237, v120
	v_add_f32_e32 v120, v238, v120
	v_add_f32_e32 v120, v239, v120
	v_add_f32_e32 v120, v240, v120
	v_add_f32_e32 v120, v241, v120
	v_add_f32_e32 v120, v242, v120
	s_waitcnt lgkmcnt(5)
	v_mfma_f32_32x32x16_bf16 v[128:143], v[172:175], v[152:155], v[128:143]
	v_add_f32_e32 v120, v243, v120
	v_add_f32_e32 v120, v244, v120
	v_add_f32_e32 v120, v245, v120
	v_add_f32_e32 v120, v246, v120
	v_add_f32_e32 v120, v247, v120
	v_add_f32_e32 v120, v248, v120
	v_add_f32_e32 v120, v112, v120
	s_waitcnt lgkmcnt(4)
	v_mfma_f32_32x32x16_bf16 v[96:111], v[176:179], v[152:155], v[96:111]
	v_add_f32_e32 v120, v113, v120
	v_add_f32_e32 v120, v114, v120
	v_add_f32_e32 v120, v115, v120
	v_add_f32_e32 v120, v116, v120
	v_exp_f32_e32 v169, v121
	v_add_f32_e32 v120, v117, v120
	v_exp_f32_e32 v170, v122
	s_waitcnt lgkmcnt(3)
	v_mfma_f32_32x32x16_bf16 v[128:143], v[218:221], v[148:151], v[128:143]
	v_add_f32_e32 v120, v118, v120
	v_exp_f32_e32 v171, v123
	v_add_f32_e32 v120, v119, v120
	v_exp_f32_e32 v172, v124
	v_add_f32_e32 v120, v168, v120
	v_exp_f32_e32 v173, v125
	v_add_f32_e32 v120, v169, v120
	s_waitcnt lgkmcnt(2)
	v_mfma_f32_32x32x16_bf16 v[96:111], v[222:225], v[148:151], v[96:111]
	v_exp_f32_e32 v174, v126
	v_add_f32_e32 v120, v170, v120
	v_exp_f32_e32 v175, v127
	v_add_f32_e32 v120, v171, v120
	v_add_f32_e32 v120, v172, v120
	v_add_f32_e32 v120, v173, v120
	v_add_f32_e32 v120, v174, v120
	s_waitcnt lgkmcnt(1)
	v_mfma_f32_32x32x16_bf16 v[128:143], v[226:229], v[144:147], v[128:143]
	v_add_f32_e32 v217, v175, v120
	v_cvt_pk_bf16_f32 v120, v182, v234
	v_cvt_pk_bf16_f32 v121, v235, v236
	v_cvt_pk_bf16_f32 v122, v237, v238
	v_cvt_pk_bf16_f32 v123, v239, v240
	v_cvt_pk_bf16_f32 v124, v241, v242
	s_waitcnt lgkmcnt(0)
	v_mfma_f32_32x32x16_bf16 v[96:111], v[230:233], v[144:147], v[96:111]
	v_lshl_add_u32 v219, s30, 14, v253
	ds_read_b64_tr_b16 v[220:221], v219 offset:0
	ds_read_b64_tr_b16 v[222:223], v219 offset:0x100
	ds_read_b64_tr_b16 v[224:225], v219 offset:0x1000
	ds_read_b64_tr_b16 v[226:227], v219 offset:0x1100
	v_cvt_pk_bf16_f32 v125, v243, v244
	v_cvt_pk_bf16_f32 v126, v245, v246
	v_cvt_pk_bf16_f32 v127, v247, v248
	v_cvt_pk_bf16_f32 v112, v112, v113
	v_cvt_pk_bf16_f32 v113, v114, v115
	v_cvt_pk_bf16_f32 v114, v116, v117
	v_cvt_pk_bf16_f32 v115, v118, v119
	v_cvt_pk_bf16_f32 v116, v168, v169
	v_cvt_pk_bf16_f32 v117, v170, v171
	v_cvt_pk_bf16_f32 v118, v172, v173
	v_cvt_pk_bf16_f32 v119, v174, v175
	s_nop 0
	s_waitcnt lgkmcnt(2)
	v_mfma_f32_32x32x16_bf16 v[48:63], v[220:223], v[120:123], v[48:63]
	s_and_b64 vcc, exec, s[2:3]
	s_cbranch_vccnz .LBB4_798
	s_mov_b64 s[2:3], s[8:9]
	global_store_dwordx2 v193, v[184:185], s[2:3] nt
; #define AT_SBAR() __builtin_amdgcn_sched_barrier(0)
; template <int OFF> DI s16x4 tr_read(int vb) { s16x4 r; asm volatile("ds_read_b64_tr_b16 %0, %1 offset:%2" : "=&v"(r) : "v"(vb), "i"(OFF) : "memory"); return r; }
; template <int D0> DI void pv_one(f32x16& od, int vb, bf16x8 pa0, bf16x8 pa1, bf16x8 pa2, bf16x8 pa3) {
;     const s16x4 l0 = tr_read<v_rd_off(D0, 0, 0)>(vb), h0 = tr_read<v_rd_off(D0, 0, 1)>(vb), l1 = tr_read<v_rd_off(D0, 1, 0)>(vb), h1 = tr_read<v_rd_off(D0, 1, 1)>(vb);
;     const s16x4 l2 = tr_read<v_rd_off(D0, 2, 0)>(vb), h2 = tr_read<v_rd_off(D0, 2, 1)>(vb), l3 = tr_read<v_rd_off(D0, 3, 0)>(vb), h3 = tr_read<v_rd_off(D0, 3, 1)>(vb);
;     asm volatile("s_waitcnt lgkmcnt(0)" ::: "memory"); AT_SBAR();
;     ...
;     od = __builtin_amdgcn_mfma_f32_32x32x16_bf16(AT_PK(l0, h0), pa0, od, 0, 0, 0);
;     od = __builtin_amdgcn_mfma_f32_32x32x16_bf16(AT_PK(l1, h1), pa1, od, 0, 0, 0);
;     od = __builtin_amdgcn_mfma_f32_32x32x16_bf16(AT_PK(l2, h2), pa2, od, 0, 0, 0);
;     od = __builtin_amdgcn_mfma_f32_32x32x16_bf16(AT_PK(l3, h3), pa3, od, 0, 0, 0);
;     ...
; }
; DI void pv_all_sm(f32x16* o, int vb, bf16x8 pa0, bf16x8 pa1, bf16x8 pa2, bf16x8 pa3, f32x16& p0, f32x16& p1, float& m_ref, f32x16& negm, float& alpha) {
;     pv_one<0>(o[0], vb, pa0, pa1, pa2, pa3);
;     float pmax = p0[0];
; #pragma unroll
;     for (int r = 1; r < 16; ++r) pmax = fmaxf(pmax, p0[r]);
;     pv_one<1>(o[1], vb, pa0, pa1, pa2, pa3);
; #pragma unroll
;     for (int r = 0; r < 16; ++r) pmax = fmaxf(pmax, p1[r]);
;     { auto rr = __builtin_amdgcn_permlane32_swap(__float_as_uint(pmax), __float_as_uint(pmax), false, false); pmax = fmaxf(__uint_as_float(rr[0]), __uint_as_float(rr[1])); }
;     pv_one<2>(o[2], vb, pa0, pa1, pa2, pa3);
;     alpha = 1.f;
;     if (__builtin_expect(!__all(pmax <= THRL), 0)) {
;         const float dl = fmaxf(pmax, 0.f); m_ref += dl; alpha = __builtin_amdgcn_exp2f(-dl);
; #pragma unroll
;         for (int r = 0; r < 16; ++r) { p0[r] -= dl; p1[r] -= dl; }
; #pragma unroll
;         for (int r = 0; r < 16; ++r) negm[r] = -m_ref;
;     }
;     pv_one<3>(o[3], vb, pa0, pa1, pa2, pa3);
; #pragma unroll
;     for (int r = 0; r < 16; ++r) p0[r] = __builtin_amdgcn_exp2f(p0[r]);
; }
.LBB4_798:
	ds_read_b64_tr_b16 v[228:229], v219 offset:0x2000
	ds_read_b64_tr_b16 v[230:231], v219 offset:0x2100
	ds_read_b64_tr_b16 v[232:233], v219 offset:0x3000
	ds_read_b64_tr_b16 v[234:235], v219 offset:0x3100
	s_waitcnt lgkmcnt(0)
	v_max_f32_e32 v182, v128, v129
	ds_read_b64_tr_b16 v[220:221], v219 offset:0x200
	ds_read_b64_tr_b16 v[222:223], v219 offset:0x300
	v_max3_f32 v182, v182, v130, v131
	v_max3_f32 v182, v182, v132, v133
	v_mfma_f32_32x32x16_bf16 v[48:63], v[224:227], v[124:127], v[48:63]
	ds_read_b64_tr_b16 v[224:225], v219 offset:0x1200
	ds_read_b64_tr_b16 v[226:227], v219 offset:0x1300
	v_max3_f32 v182, v182, v134, v135
	v_max3_f32 v182, v182, v136, v137
	v_max3_f32 v182, v182, v138, v139
	v_max3_f32 v182, v182, v140, v141
	v_max3_f32 v182, v182, v142, v143
	v_mfma_f32_32x32x16_bf16 v[48:63], v[228:231], v[112:115], v[48:63]
	ds_read_b64_tr_b16 v[228:229], v219 offset:0x2200
	ds_read_b64_tr_b16 v[230:231], v219 offset:0x2300
	ds_read_b64_tr_b16 v[236:237], v219 offset:0x3200
	ds_read_b64_tr_b16 v[238:239], v219 offset:0x3300
	v_mfma_f32_32x32x16_bf16 v[48:63], v[232:235], v[116:119], v[48:63]
	s_waitcnt lgkmcnt(0)
	v_mfma_f32_32x32x16_bf16 v[32:47], v[220:223], v[120:123], v[32:47]
	v_max3_f32 v182, v182, v96, v97
	v_max3_f32 v182, v182, v98, v99
	ds_read_b64_tr_b16 v[222:223], v219 offset:0x400
	v_max3_f32 v182, v182, v100, v101
	v_max3_f32 v182, v182, v102, v103
	v_max3_f32 v182, v182, v104, v105
	v_max3_f32 v182, v182, v106, v107
	v_mfma_f32_32x32x16_bf16 v[32:47], v[224:227], v[124:127], v[32:47]
	ds_read_b64_tr_b16 v[224:225], v219 offset:0x500
	ds_read_b64_tr_b16 v[226:227], v219 offset:0x1400
	v_max3_f32 v182, v182, v108, v109
	v_max3_f32 v182, v182, v110, v111
	v_mov_b32_e32 v220, v182
	s_nop 1
	v_permlane32_swap_b32_e32 v182, v220
	v_mfma_f32_32x32x16_bf16 v[32:47], v[228:231], v[112:115], v[32:47]
	ds_read_b64_tr_b16 v[228:229], v219 offset:0x1500
	ds_read_b64_tr_b16 v[230:231], v219 offset:0x2400
	ds_read_b64_tr_b16 v[232:233], v219 offset:0x2500
	ds_read_b64_tr_b16 v[240:241], v219 offset:0x3400
	ds_read_b64_tr_b16 v[242:243], v219 offset:0x3500
	v_mfma_f32_32x32x16_bf16 v[32:47], v[236:239], v[116:119], v[32:47]
	s_waitcnt lgkmcnt(0)
	v_max_f32_e32 v220, v182, v220
	v_mfma_f32_32x32x16_bf16 v[16:31], v[222:225], v[120:123], v[16:31]
	v_cmp_ge_f32_e32 vcc, s26, v220
	s_cmp_eq_u64 vcc, exec
	v_mov_b32_e32 v182, 1.0
	v_mfma_f32_32x32x16_bf16 v[16:31], v[226:229], v[124:127], v[16:31]
	v_mfma_f32_32x32x16_bf16 v[16:31], v[230:233], v[112:115], v[16:31]
	v_mfma_f32_32x32x16_bf16 v[16:31], v[240:243], v[116:119], v[16:31]
	s_cbranch_scc0 .LBB4_811

; DI void finishSM(f32x16& p0, f32x16& p1, float alpha, float& l_reg, bf16x8& pa0, bf16x8& pa1, bf16x8& pa2, bf16x8& pa3) {
; #pragma unroll
;     for (int r = 0; r < 16; ++r) p1[r] = __builtin_amdgcn_exp2f(p1[r]);
;     float ps = 0;
; #pragma unroll
;     for (int r = 0; r < 16; ++r) ps += p0[r];
; #pragma unroll
;     for (int r = 0; r < 16; ++r) ps += p1[r];
;     { auto rr = __builtin_amdgcn_permlane32_swap(__float_as_uint(ps), __float_as_uint(ps), false, false); ps = __uint_as_float(rr[0]) + __uint_as_float(rr[1]); }
;     l_reg = l_reg * alpha + ps;
;     ...
;     AT_PK4(p0, 0, pa0); AT_PK4(p0, 8, pa1); AT_PK4(p1, 0, pa2); AT_PK4(p1, 8, pa3);
;     ...
; }
; DI void qkt(f32x16& p0, f32x16& p1, const char* Ks, const bf16x8* qr, const f32x16& negm, int r32, int hi) {
; #pragma unroll
;     for (int d0 = 0; d0 < 4; ++d0) { const int cb = (d0 * 16 + hi * 8) * 2;
;         const bf16x8 b0 = *reinterpret_cast<const bf16x8*>(Ks + AT_KSWZ(r32, cb));
;         const bf16x8 b1 = *reinterpret_cast<const bf16x8*>(Ks + AT_KSWZ(32 + r32, cb));
;         p0 = __builtin_amdgcn_mfma_f32_32x32x16_bf16(b0, qr[d0], d0 == 0 ? negm : p0, 0, 0, 0);
;         p1 = __builtin_amdgcn_mfma_f32_32x32x16_bf16(b1, qr[d0], d0 == 0 ? negm : p1, 0, 0, 0); }
; }
; template <int D0> DI void pv_one(f32x16& od, int vb, bf16x8 pa0, bf16x8 pa1, bf16x8 pa2, bf16x8 pa3) {
;     const s16x4 l0 = tr_read<v_rd_off(D0, 0, 0)>(vb), h0 = tr_read<v_rd_off(D0, 0, 1)>(vb), l1 = tr_read<v_rd_off(D0, 1, 0)>(vb), h1 = tr_read<v_rd_off(D0, 1, 1)>(vb);
;     const s16x4 l2 = tr_read<v_rd_off(D0, 2, 0)>(vb), h2 = tr_read<v_rd_off(D0, 2, 1)>(vb), l3 = tr_read<v_rd_off(D0, 3, 0)>(vb), h3 = tr_read<v_rd_off(D0, 3, 1)>(vb);
;     asm volatile("s_waitcnt lgkmcnt(0)" ::: "memory"); AT_SBAR();
;     ...
;     od = __builtin_amdgcn_mfma_f32_32x32x16_bf16(AT_PK(l0, h0), pa0, od, 0, 0, 0);
;     od = __builtin_amdgcn_mfma_f32_32x32x16_bf16(AT_PK(l1, h1), pa1, od, 0, 0, 0);
;     od = __builtin_amdgcn_mfma_f32_32x32x16_bf16(AT_PK(l2, h2), pa2, od, 0, 0, 0);
;     od = __builtin_amdgcn_mfma_f32_32x32x16_bf16(AT_PK(l3, h3), pa3, od, 0, 0, 0);
;     ...
; }
; DI void pv_all_sm(f32x16* o, int vb, bf16x8 pa0, bf16x8 pa1, bf16x8 pa2, bf16x8 pa3, f32x16& p0, f32x16& p1, float& m_ref, f32x16& negm, float& alpha) {
;     pv_one<0>(o[0], vb, pa0, pa1, pa2, pa3);
;     float pmax = p0[0];
; #pragma unroll
;     for (int r = 1; r < 16; ++r) pmax = fmaxf(pmax, p0[r]);
.LBB4_849:
	s_lshl_b32 s26, s64, 13
	s_add_i32 s26, s26, 0
	v_add_u32_e32 v72, s26, v204
	v_add_u32_e32 v112, s26, v205
	v_add_u32_e32 v180, s26, v206
	s_waitcnt lgkmcnt(1)
	v_mfma_f32_32x32x16_bf16 v[128:143], v[64:67], v[156:159], v[80:95]
	ds_read_b128 v[64:67], v72 offset:49152
	ds_read_b128 v[72:75], v72 offset:53248
	ds_read_b128 v[76:79], v112 offset:49152
	ds_read_b128 v[220:223], v112 offset:53248
	s_add_u32 s66, s46, s28
	s_addc_u32 s67, s47, s29
	s_add_u32 s34, s66, 0x23808000
	s_addc_u32 s35, s67, 0
	s_add_u32 s76, s66, 0x2380a000
	s_add_u32 s74, s46, s24
	s_addc_u32 s75, s47, s25
	s_add_u32 s78, s74, 0x21804000
	s_addc_u32 s79, s75, 0
	s_lshl_b32 s92, s57, 14
	s_add_i32 s92, s92, s94
	s_mov_b32 m0, s92
	s_lshl_b32 s96, s57, 13
	global_load_lds_dwordx4 v249, s[34:35]
	s_addk_i32 s92, 0x400
	s_mov_b32 m0, s92
	s_add_i32 s96, s96, s95
	global_load_lds_dwordx4 v250, s[34:35]
	s_nop 0
	s_mov_b32 m0, s96
	s_nop 0
	global_load_lds_dwordx4 v251, s[78:79]
	v_exp_f32_e32 v182, v97
	v_exp_f32_e32 v213, v98
	v_exp_f32_e32 v214, v99
	v_exp_f32_e32 v219, v100
	v_exp_f32_e32 v228, v101
	s_waitcnt lgkmcnt(4)
	v_mfma_f32_32x32x16_bf16 v[112:127], v[68:71], v[156:159], v[80:95]
	ds_read_b128 v[68:71], v180 offset:49152
	ds_read_b128 v[224:227], v180 offset:53248
	v_exp_f32_e32 v180, v96
	v_cvt_pk_bf16_f32 v96, v216, v218
	v_cvt_pk_bf16_f32 v97, v179, v217
	v_cvt_pk_bf16_f32 v98, v177, v215
	v_cvt_pk_bf16_f32 v99, v176, v178
	s_waitcnt lgkmcnt(4)
	v_mfma_f32_32x32x16_bf16 v[112:127], v[72:75], v[152:155], v[112:127]
	v_add_f32_e32 v75, 0, v216
	v_add_f32_e32 v75, v218, v75
	v_add_f32_e32 v75, v179, v75
	v_add_f32_e32 v75, v217, v75
	v_add_f32_e32 v75, v177, v75
	v_add_f32_e32 v75, v215, v75
	v_add_f32_e32 v75, v176, v75
	v_mfma_f32_32x32x16_bf16 v[128:143], v[64:67], v[152:155], v[128:143]
	v_add_f32_e32 v75, v178, v75
	v_add_f32_e32 v75, v173, v75
	v_add_f32_e32 v75, v175, v75
	v_add_f32_e32 v75, v171, v75
	v_add_f32_e32 v75, v174, v75
	v_add_f32_e32 v75, v169, v75
	v_add_f32_e32 v75, v172, v75
	s_waitcnt lgkmcnt(3)
	v_mfma_f32_32x32x16_bf16 v[128:143], v[76:79], v[148:151], v[128:143]
	v_add_f32_e32 v75, v168, v75
	v_add_f32_e32 v75, v170, v75
	v_add_f32_e32 v75, v180, v75
	v_add_f32_e32 v75, v182, v75
	v_exp_f32_e32 v64, v102
	v_exp_f32_e32 v65, v103
	v_exp_f32_e32 v66, v104
	s_waitcnt lgkmcnt(2)
	v_mfma_f32_32x32x16_bf16 v[112:127], v[220:223], v[148:151], v[112:127]
	v_exp_f32_e32 v67, v105
	v_exp_f32_e32 v105, v106
	v_exp_f32_e32 v106, v107
	v_exp_f32_e32 v107, v108
	v_exp_f32_e32 v72, v109
	v_exp_f32_e32 v73, v110
	v_exp_f32_e32 v74, v111
	s_waitcnt lgkmcnt(1)
	v_mfma_f32_32x32x16_bf16 v[128:143], v[68:71], v[144:147], v[128:143]
	v_add_f32_e32 v68, v213, v75
	v_add_f32_e32 v68, v214, v68
	v_add_f32_e32 v68, v219, v68
	v_add_f32_e32 v68, v228, v68
	v_add_f32_e32 v68, v64, v68
	v_add_f32_e32 v68, v65, v68
	v_add_f32_e32 v68, v66, v68
	v_add_f32_e32 v68, v67, v68
	s_waitcnt lgkmcnt(0)
	v_mfma_f32_32x32x16_bf16 v[112:127], v[224:227], v[144:147], v[112:127]
	v_cvt_pk_bf16_f32 v100, v180, v182
	v_cvt_pk_bf16_f32 v103, v64, v65
	v_cvt_pk_bf16_f32 v104, v66, v67
	s_lshl_b32 s65, s63, 14
	v_add_u32_e32 v182, s65, v253
	ds_read_b64_tr_b16 v[64:65], v182 offset:0
	ds_read_b64_tr_b16 v[66:67], v182 offset:0x100
	v_add_f32_e32 v68, v105, v68
	v_add_f32_e32 v68, v106, v68
	v_add_f32_e32 v68, v107, v68
	v_add_f32_e32 v68, v72, v68
	v_add_f32_e32 v68, v73, v68
	v_add_f32_e32 v211, v74, v68
	ds_read_b64_tr_b16 v[68:69], v182 offset:0x1000
	ds_read_b64_tr_b16 v[70:71], v182 offset:0x1100
	v_cvt_pk_bf16_f32 v108, v173, v175
	v_cvt_pk_bf16_f32 v109, v171, v174
	v_cvt_pk_bf16_f32 v110, v169, v172
	v_cvt_pk_bf16_f32 v111, v168, v170
	v_cvt_pk_bf16_f32 v101, v213, v214
	v_cvt_pk_bf16_f32 v102, v219, v228
	v_cvt_pk_bf16_f32 v105, v105, v106
	v_cvt_pk_bf16_f32 v106, v107, v72
	v_cvt_pk_bf16_f32 v107, v73, v74
	s_nop 0
	s_waitcnt lgkmcnt(2)
	v_mfma_f32_32x32x16_bf16 v[32:47], v[64:67], v[96:99], v[32:47]
	s_addc_u32 s77, s67, 0
	s_andn2_b64 vcc, exec, s[2:3]
	s_cbranch_vccnz .LBB4_851
	s_mov_b64 s[2:3], s[8:9]
	global_store_dwordx2 v188, v[184:185], s[2:3] nt
.LBB4_851:
	ds_read_b64_tr_b16 v[72:73], v182 offset:0x2000
	ds_read_b64_tr_b16 v[74:75], v182 offset:0x2100
	ds_read_b64_tr_b16 v[76:77], v182 offset:0x3000
	ds_read_b64_tr_b16 v[78:79], v182 offset:0x3100
	s_waitcnt lgkmcnt(0)
	v_max_f32_e32 v64, v128, v129
	v_max3_f32 v64, v64, v130, v131
	v_max3_f32 v64, v64, v132, v133
	v_max3_f32 v64, v64, v134, v135
	v_max3_f32 v64, v64, v136, v137
	v_mfma_f32_32x32x16_bf16 v[32:47], v[68:71], v[108:111], v[32:47]
	v_max3_f32 v64, v64, v138, v139
	v_max3_f32 v66, v64, v140, v141
	ds_read_b64_tr_b16 v[64:65], v182 offset:0x200
	v_max3_f32 v180, v66, v142, v143
	ds_read_b64_tr_b16 v[66:67], v182 offset:0x300
	ds_read_b64_tr_b16 v[68:69], v182 offset:0x1200
	ds_read_b64_tr_b16 v[70:71], v182 offset:0x1300
	v_mfma_f32_32x32x16_bf16 v[32:47], v[72:75], v[100:103], v[32:47]
	ds_read_b64_tr_b16 v[72:73], v182 offset:0x2200
	ds_read_b64_tr_b16 v[74:75], v182 offset:0x2300
	ds_read_b64_tr_b16 v[214:215], v182 offset:0x3200
	ds_read_b64_tr_b16 v[216:217], v182 offset:0x3300
	v_mfma_f32_32x32x16_bf16 v[32:47], v[76:79], v[104:107], v[32:47]
	s_waitcnt lgkmcnt(0)
	v_mfma_f32_32x32x16_bf16 v[48:63], v[64:67], v[96:99], v[48:63]
	v_max3_f32 v76, v180, v112, v113
	v_max3_f32 v64, v76, v114, v115
	ds_read_b64_tr_b16 v[66:67], v182 offset:0x400
	v_max3_f32 v64, v64, v116, v117
	v_max3_f32 v64, v64, v118, v119
	v_max3_f32 v64, v64, v120, v121
	v_max3_f32 v64, v64, v122, v123
	v_mfma_f32_32x32x16_bf16 v[48:63], v[68:71], v[108:111], v[48:63]
	ds_read_b64_tr_b16 v[68:69], v182 offset:0x500
	ds_read_b64_tr_b16 v[70:71], v182 offset:0x1400
	v_max3_f32 v64, v64, v124, v125
	v_max3_f32 v64, v64, v126, v127
	v_mov_b32_e32 v65, v64
	s_nop 1
	v_permlane32_swap_b32_e32 v64, v65
	v_mfma_f32_32x32x16_bf16 v[48:63], v[72:75], v[100:103], v[48:63]
	ds_read_b64_tr_b16 v[72:73], v182 offset:0x1500
	ds_read_b64_tr_b16 v[74:75], v182 offset:0x2400
	ds_read_b64_tr_b16 v[76:77], v182 offset:0x2500
	ds_read_b64_tr_b16 v[218:219], v182 offset:0x3400
	ds_read_b64_tr_b16 v[220:221], v182 offset:0x3500
	v_mfma_f32_32x32x16_bf16 v[48:63], v[214:217], v[104:107], v[48:63]
	s_waitcnt lgkmcnt(0)
	v_max_f32_e32 v64, v64, v65
	v_mfma_f32_32x32x16_bf16 v[16:31], v[66:69], v[96:99], v[16:31]
	v_cmp_ge_f32_e32 vcc, s15, v64
	s_cmp_eq_u64 vcc, exec
	v_mfma_f32_32x32x16_bf16 v[16:31], v[70:73], v[108:111], v[16:31]
	v_mfma_f32_32x32x16_bf16 v[16:31], v[74:77], v[100:103], v[16:31]
	v_mfma_f32_32x32x16_bf16 v[16:31], v[218:221], v[104:107], v[16:31]
	s_cbranch_scc0 .LBB4_884
	v_mov_b32_e32 v180, 1.0

; #define AT_SBAR() __builtin_amdgcn_sched_barrier(0)
; template <int OFF> DI s16x4 tr_read(int vb) { s16x4 r; asm volatile("ds_read_b64_tr_b16 %0, %1 offset:%2" : "=&v"(r) : "v"(vb), "i"(OFF) : "memory"); return r; }
; DI void finishSM(f32x16& p0, f32x16& p1, float alpha, float& l_reg, bf16x8& pa0, bf16x8& pa1, bf16x8& pa2, bf16x8& pa3) {
; #pragma unroll
;     for (int r = 0; r < 16; ++r) p1[r] = __builtin_amdgcn_exp2f(p1[r]);
;     float ps = 0;
; #pragma unroll
;     for (int r = 0; r < 16; ++r) ps += p0[r];
; #pragma unroll
;     for (int r = 0; r < 16; ++r) ps += p1[r];
;     { auto rr = __builtin_amdgcn_permlane32_swap(__float_as_uint(ps), __float_as_uint(ps), false, false); ps = __uint_as_float(rr[0]) + __uint_as_float(rr[1]); }
;     l_reg = l_reg * alpha + ps;
;     ...
;     AT_PK4(p0, 0, pa0); AT_PK4(p0, 8, pa1); AT_PK4(p1, 0, pa2); AT_PK4(p1, 8, pa3);
;     ...
; }
; DI void qkt(f32x16& p0, f32x16& p1, const char* Ks, const bf16x8* qr, const f32x16& negm, int r32, int hi) {
; #pragma unroll
;     for (int d0 = 0; d0 < 4; ++d0) { const int cb = (d0 * 16 + hi * 8) * 2;
;         const bf16x8 b0 = *reinterpret_cast<const bf16x8*>(Ks + AT_KSWZ(r32, cb));
;         const bf16x8 b1 = *reinterpret_cast<const bf16x8*>(Ks + AT_KSWZ(32 + r32, cb));
;         p0 = __builtin_amdgcn_mfma_f32_32x32x16_bf16(b0, qr[d0], d0 == 0 ? negm : p0, 0, 0, 0);
;         p1 = __builtin_amdgcn_mfma_f32_32x32x16_bf16(b1, qr[d0], d0 == 0 ? negm : p1, 0, 0, 0); }
; }
; template <int D0> DI void pv_one(f32x16& od, int vb, bf16x8 pa0, bf16x8 pa1, bf16x8 pa2, bf16x8 pa3) {
;     const s16x4 l0 = tr_read<v_rd_off(D0, 0, 0)>(vb), h0 = tr_read<v_rd_off(D0, 0, 1)>(vb), l1 = tr_read<v_rd_off(D0, 1, 0)>(vb), h1 = tr_read<v_rd_off(D0, 1, 1)>(vb);
;     const s16x4 l2 = tr_read<v_rd_off(D0, 2, 0)>(vb), h2 = tr_read<v_rd_off(D0, 2, 1)>(vb), l3 = tr_read<v_rd_off(D0, 3, 0)>(vb), h3 = tr_read<v_rd_off(D0, 3, 1)>(vb);
;     asm volatile("s_waitcnt lgkmcnt(0)" ::: "memory"); AT_SBAR();
;     ...
;     od = __builtin_amdgcn_mfma_f32_32x32x16_bf16(AT_PK(l0, h0), pa0, od, 0, 0, 0);
;     od = __builtin_amdgcn_mfma_f32_32x32x16_bf16(AT_PK(l1, h1), pa1, od, 0, 0, 0);
;     od = __builtin_amdgcn_mfma_f32_32x32x16_bf16(AT_PK(l2, h2), pa2, od, 0, 0, 0);
;     od = __builtin_amdgcn_mfma_f32_32x32x16_bf16(AT_PK(l3, h3), pa3, od, 0, 0, 0);
;     ...
; }
.LBB4_870:
	v_exp_f32_e32 v182, v128
	v_exp_f32_e32 v230, v129
	v_exp_f32_e32 v231, v130
	v_exp_f32_e32 v232, v131
	v_exp_f32_e32 v233, v132
	v_exp_f32_e32 v234, v133
	v_exp_f32_e32 v235, v134
	v_exp_f32_e32 v236, v135
	v_exp_f32_e32 v237, v136
	v_exp_f32_e32 v238, v137
	v_exp_f32_e32 v239, v138
	v_exp_f32_e32 v240, v139
	v_exp_f32_e32 v241, v140
	v_exp_f32_e32 v242, v141
	v_exp_f32_e32 v243, v142
	v_exp_f32_e32 v244, v143
	v_add_u32_e32 v101, s76, v204
	v_add_u32_e32 v102, s76, v205
	v_add_u32_e32 v103, s76, v206
	ds_read_b128 v[172:175], v101 offset:49152
	ds_read_b128 v[176:179], v101 offset:53248
	ds_read_b128 v[214:217], v102 offset:49152
	ds_read_b128 v[218:221], v102 offset:53248
	ds_read_b128 v[222:225], v103 offset:49152
	ds_read_b128 v[226:229], v103 offset:53248
	v_exp_f32_e32 v112, v112
	v_exp_f32_e32 v113, v113
	v_exp_f32_e32 v114, v114
	s_waitcnt lgkmcnt(7)
	v_mfma_f32_32x32x16_bf16 v[128:143], v[96:99], v[156:159], v[80:95]
	s_add_u32 s34, s66, 0x2380c000
	s_addc_u32 s35, s67, 0
	s_add_u32 s66, s66, 0x2380e000
	s_addc_u32 s67, s67, 0
	s_add_u32 s74, s74, 0x21806000
	s_addc_u32 s75, s75, 0
	s_lshl_b32 s92, s63, 14
	s_add_i32 s92, s92, s94
	s_mov_b32 m0, s92
	s_lshl_b32 s96, s63, 13
	global_load_lds_dwordx4 v249, s[34:35]
	s_addk_i32 s92, 0x400
	s_mov_b32 m0, s92
	s_add_i32 s96, s96, s95
	global_load_lds_dwordx4 v250, s[34:35]
	s_nop 0
	s_mov_b32 m0, s96
	s_nop 0
	global_load_lds_dwordx4 v251, s[74:75]
	s_nop 0
	v_exp_f32_e32 v115, v115
	v_exp_f32_e32 v116, v116
	v_exp_f32_e32 v117, v117
	v_exp_f32_e32 v118, v118
	v_exp_f32_e32 v119, v119
	s_waitcnt lgkmcnt(6)
	v_mfma_f32_32x32x16_bf16 v[96:111], v[168:171], v[156:159], v[80:95]
	v_exp_f32_e32 v168, v120
	v_add_f32_e32 v120, 0, v182
	v_add_f32_e32 v120, v230, v120
	v_add_f32_e32 v120, v231, v120
	v_add_f32_e32 v120, v232, v120
	v_add_f32_e32 v120, v233, v120
	v_add_f32_e32 v120, v234, v120
	v_add_f32_e32 v120, v235, v120
	v_add_f32_e32 v120, v236, v120
	v_add_f32_e32 v120, v237, v120
	v_add_f32_e32 v120, v238, v120
	s_waitcnt lgkmcnt(5)
	v_mfma_f32_32x32x16_bf16 v[128:143], v[172:175], v[152:155], v[128:143]
	v_add_f32_e32 v120, v239, v120
	v_add_f32_e32 v120, v240, v120
	v_add_f32_e32 v120, v241, v120
	v_add_f32_e32 v120, v242, v120
	v_add_f32_e32 v120, v243, v120
	v_add_f32_e32 v120, v244, v120
	v_add_f32_e32 v120, v112, v120
	s_waitcnt lgkmcnt(4)
	v_mfma_f32_32x32x16_bf16 v[96:111], v[176:179], v[152:155], v[96:111]
	v_add_f32_e32 v120, v113, v120
	v_add_f32_e32 v120, v114, v120
	v_add_f32_e32 v120, v115, v120
	v_add_f32_e32 v120, v116, v120
	v_exp_f32_e32 v169, v121
	v_add_f32_e32 v120, v117, v120
	v_exp_f32_e32 v170, v122
	s_waitcnt lgkmcnt(3)
	v_mfma_f32_32x32x16_bf16 v[128:143], v[214:217], v[148:151], v[128:143]
	v_add_f32_e32 v120, v118, v120
	v_exp_f32_e32 v171, v123
	v_add_f32_e32 v120, v119, v120
	v_exp_f32_e32 v172, v124
	v_add_f32_e32 v120, v168, v120
	v_exp_f32_e32 v173, v125
	v_add_f32_e32 v120, v169, v120
	s_waitcnt lgkmcnt(2)
	v_mfma_f32_32x32x16_bf16 v[96:111], v[218:221], v[148:151], v[96:111]
	v_exp_f32_e32 v174, v126
	v_add_f32_e32 v120, v170, v120
	v_exp_f32_e32 v175, v127
	v_add_f32_e32 v120, v171, v120
	v_add_f32_e32 v120, v172, v120
	v_add_f32_e32 v120, v173, v120
	v_add_f32_e32 v120, v174, v120
	s_waitcnt lgkmcnt(1)
	v_mfma_f32_32x32x16_bf16 v[128:143], v[222:225], v[144:147], v[128:143]
	v_add_f32_e32 v213, v175, v120
	v_cvt_pk_bf16_f32 v120, v182, v230
	v_cvt_pk_bf16_f32 v121, v231, v232
	v_cvt_pk_bf16_f32 v122, v233, v234
	v_cvt_pk_bf16_f32 v123, v235, v236
	v_cvt_pk_bf16_f32 v124, v237, v238
	s_waitcnt lgkmcnt(0)
	v_mfma_f32_32x32x16_bf16 v[96:111], v[226:229], v[144:147], v[96:111]
	v_lshl_add_u32 v215, s64, 14, v253
	ds_read_b64_tr_b16 v[216:217], v215 offset:0
	ds_read_b64_tr_b16 v[218:219], v215 offset:0x100
	ds_read_b64_tr_b16 v[220:221], v215 offset:0x1000
	ds_read_b64_tr_b16 v[222:223], v215 offset:0x1100
	v_cvt_pk_bf16_f32 v125, v239, v240
	v_cvt_pk_bf16_f32 v126, v241, v242
	v_cvt_pk_bf16_f32 v127, v243, v244
	v_cvt_pk_bf16_f32 v112, v112, v113
	v_cvt_pk_bf16_f32 v113, v114, v115
	v_cvt_pk_bf16_f32 v114, v116, v117
	v_cvt_pk_bf16_f32 v115, v118, v119
	v_cvt_pk_bf16_f32 v116, v168, v169
	v_cvt_pk_bf16_f32 v117, v170, v171
	v_cvt_pk_bf16_f32 v118, v172, v173
	v_cvt_pk_bf16_f32 v119, v174, v175
	s_nop 0
	s_waitcnt lgkmcnt(2)
	v_mfma_f32_32x32x16_bf16 v[32:47], v[216:219], v[120:123], v[32:47]
	s_and_b64 vcc, exec, s[2:3]
	s_cbranch_vccnz .LBB4_872
	s_mov_b64 s[2:3], s[8:9]
	global_store_dwordx2 v188, v[184:185], s[2:3] nt
; #define AT_SBAR() __builtin_amdgcn_sched_barrier(0)
; template <int OFF> DI s16x4 tr_read(int vb) { s16x4 r; asm volatile("ds_read_b64_tr_b16 %0, %1 offset:%2" : "=&v"(r) : "v"(vb), "i"(OFF) : "memory"); return r; }
; template <int D0> DI void pv_one(f32x16& od, int vb, bf16x8 pa0, bf16x8 pa1, bf16x8 pa2, bf16x8 pa3) {
;     const s16x4 l0 = tr_read<v_rd_off(D0, 0, 0)>(vb), h0 = tr_read<v_rd_off(D0, 0, 1)>(vb), l1 = tr_read<v_rd_off(D0, 1, 0)>(vb), h1 = tr_read<v_rd_off(D0, 1, 1)>(vb);
;     const s16x4 l2 = tr_read<v_rd_off(D0, 2, 0)>(vb), h2 = tr_read<v_rd_off(D0, 2, 1)>(vb), l3 = tr_read<v_rd_off(D0, 3, 0)>(vb), h3 = tr_read<v_rd_off(D0, 3, 1)>(vb);
;     asm volatile("s_waitcnt lgkmcnt(0)" ::: "memory"); AT_SBAR();
;     ...
;     od = __builtin_amdgcn_mfma_f32_32x32x16_bf16(AT_PK(l0, h0), pa0, od, 0, 0, 0);
;     od = __builtin_amdgcn_mfma_f32_32x32x16_bf16(AT_PK(l1, h1), pa1, od, 0, 0, 0);
;     od = __builtin_amdgcn_mfma_f32_32x32x16_bf16(AT_PK(l2, h2), pa2, od, 0, 0, 0);
;     od = __builtin_amdgcn_mfma_f32_32x32x16_bf16(AT_PK(l3, h3), pa3, od, 0, 0, 0);
;     ...
; }
; DI void pv_all_sm(f32x16* o, int vb, bf16x8 pa0, bf16x8 pa1, bf16x8 pa2, bf16x8 pa3, f32x16& p0, f32x16& p1, float& m_ref, f32x16& negm, float& alpha) {
;     pv_one<0>(o[0], vb, pa0, pa1, pa2, pa3);
;     float pmax = p0[0];
; #pragma unroll
;     for (int r = 1; r < 16; ++r) pmax = fmaxf(pmax, p0[r]);
;     pv_one<1>(o[1], vb, pa0, pa1, pa2, pa3);
; #pragma unroll
;     for (int r = 0; r < 16; ++r) pmax = fmaxf(pmax, p1[r]);
;     { auto rr = __builtin_amdgcn_permlane32_swap(__float_as_uint(pmax), __float_as_uint(pmax), false, false); pmax = fmaxf(__uint_as_float(rr[0]), __uint_as_float(rr[1])); }
;     pv_one<2>(o[2], vb, pa0, pa1, pa2, pa3);
;     alpha = 1.f;
;     if (__builtin_expect(!__all(pmax <= THRL), 0)) {
;         const float dl = fmaxf(pmax, 0.f); m_ref += dl; alpha = __builtin_amdgcn_exp2f(-dl);
; #pragma unroll
;         for (int r = 0; r < 16; ++r) { p0[r] -= dl; p1[r] -= dl; }
; #pragma unroll
;         for (int r = 0; r < 16; ++r) negm[r] = -m_ref;
;     }
;     pv_one<3>(o[3], vb, pa0, pa1, pa2, pa3);
; #pragma unroll
;     for (int r = 0; r < 16; ++r) p0[r] = __builtin_amdgcn_exp2f(p0[r]);
; }
.LBB4_872:
	ds_read_b64_tr_b16 v[224:225], v215 offset:0x2000
	ds_read_b64_tr_b16 v[226:227], v215 offset:0x2100
	ds_read_b64_tr_b16 v[228:229], v215 offset:0x3000
	ds_read_b64_tr_b16 v[230:231], v215 offset:0x3100
	s_waitcnt lgkmcnt(0)
	v_max_f32_e32 v182, v128, v129
	ds_read_b64_tr_b16 v[216:217], v215 offset:0x200
	ds_read_b64_tr_b16 v[218:219], v215 offset:0x300
	v_max3_f32 v182, v182, v130, v131
	v_max3_f32 v182, v182, v132, v133
	v_mfma_f32_32x32x16_bf16 v[32:47], v[220:223], v[124:127], v[32:47]
	ds_read_b64_tr_b16 v[220:221], v215 offset:0x1200
	ds_read_b64_tr_b16 v[222:223], v215 offset:0x1300
	v_max3_f32 v182, v182, v134, v135
	v_max3_f32 v182, v182, v136, v137
	v_max3_f32 v182, v182, v138, v139
	v_max3_f32 v182, v182, v140, v141
	v_max3_f32 v182, v182, v142, v143
	v_mfma_f32_32x32x16_bf16 v[32:47], v[224:227], v[112:115], v[32:47]
	ds_read_b64_tr_b16 v[224:225], v215 offset:0x2200
	ds_read_b64_tr_b16 v[226:227], v215 offset:0x2300
	ds_read_b64_tr_b16 v[232:233], v215 offset:0x3200
	ds_read_b64_tr_b16 v[234:235], v215 offset:0x3300
	v_mfma_f32_32x32x16_bf16 v[32:47], v[228:231], v[116:119], v[32:47]
	s_waitcnt lgkmcnt(0)
	v_mfma_f32_32x32x16_bf16 v[48:63], v[216:219], v[120:123], v[48:63]
	v_max3_f32 v182, v182, v96, v97
	v_max3_f32 v182, v182, v98, v99
	ds_read_b64_tr_b16 v[218:219], v215 offset:0x400
	v_max3_f32 v182, v182, v100, v101
	v_max3_f32 v182, v182, v102, v103
	v_max3_f32 v182, v182, v104, v105
	v_max3_f32 v182, v182, v106, v107
	v_mfma_f32_32x32x16_bf16 v[48:63], v[220:223], v[124:127], v[48:63]
	ds_read_b64_tr_b16 v[220:221], v215 offset:0x500
	ds_read_b64_tr_b16 v[222:223], v215 offset:0x1400
	v_max3_f32 v182, v182, v108, v109
	v_max3_f32 v182, v182, v110, v111
	v_mov_b32_e32 v216, v182
	s_nop 1
	v_permlane32_swap_b32_e32 v182, v216
	v_mfma_f32_32x32x16_bf16 v[48:63], v[224:227], v[112:115], v[48:63]
	ds_read_b64_tr_b16 v[224:225], v215 offset:0x1500
	ds_read_b64_tr_b16 v[226:227], v215 offset:0x2400
	ds_read_b64_tr_b16 v[228:229], v215 offset:0x2500
	ds_read_b64_tr_b16 v[236:237], v215 offset:0x3400
	ds_read_b64_tr_b16 v[238:239], v215 offset:0x3500
	v_mfma_f32_32x32x16_bf16 v[48:63], v[232:235], v[116:119], v[48:63]
	s_waitcnt lgkmcnt(0)
	v_max_f32_e32 v216, v182, v216
	v_mfma_f32_32x32x16_bf16 v[16:31], v[218:221], v[120:123], v[16:31]
	v_cmp_ge_f32_e32 vcc, s15, v216
	s_cmp_eq_u64 vcc, exec
	v_mov_b32_e32 v182, 1.0
	v_mfma_f32_32x32x16_bf16 v[16:31], v[222:225], v[124:127], v[16:31]
	v_mfma_f32_32x32x16_bf16 v[16:31], v[226:229], v[112:115], v[16:31]
	v_mfma_f32_32x32x16_bf16 v[16:31], v[236:239], v[116:119], v[16:31]
	s_cbranch_scc0 .LBB4_885

; #define AT_SBAR() __builtin_amdgcn_sched_barrier(0)
; template <int OFF> DI s16x4 tr_read(int vb) { s16x4 r; asm volatile("ds_read_b64_tr_b16 %0, %1 offset:%2" : "=&v"(r) : "v"(vb), "i"(OFF) : "memory"); return r; }
; DI void finishSM(f32x16& p0, f32x16& p1, float alpha, float& l_reg, bf16x8& pa0, bf16x8& pa1, bf16x8& pa2, bf16x8& pa3) {
; #pragma unroll
;     for (int r = 0; r < 16; ++r) p1[r] = __builtin_amdgcn_exp2f(p1[r]);
;     float ps = 0;
; #pragma unroll
;     for (int r = 0; r < 16; ++r) ps += p0[r];
; #pragma unroll
;     for (int r = 0; r < 16; ++r) ps += p1[r];
;     { auto rr = __builtin_amdgcn_permlane32_swap(__float_as_uint(ps), __float_as_uint(ps), false, false); ps = __uint_as_float(rr[0]) + __uint_as_float(rr[1]); }
;     l_reg = l_reg * alpha + ps;
;     ...
;     AT_PK4(p0, 0, pa0); AT_PK4(p0, 8, pa1); AT_PK4(p1, 0, pa2); AT_PK4(p1, 8, pa3);
;     ...
; }
; DI void qkt(f32x16& p0, f32x16& p1, const char* Ks, const bf16x8* qr, const f32x16& negm, int r32, int hi) {
; #pragma unroll
;     for (int d0 = 0; d0 < 4; ++d0) { const int cb = (d0 * 16 + hi * 8) * 2;
;         const bf16x8 b0 = *reinterpret_cast<const bf16x8*>(Ks + AT_KSWZ(r32, cb));
;         const bf16x8 b1 = *reinterpret_cast<const bf16x8*>(Ks + AT_KSWZ(32 + r32, cb));
;         p0 = __builtin_amdgcn_mfma_f32_32x32x16_bf16(b0, qr[d0], d0 == 0 ? negm : p0, 0, 0, 0);
;         p1 = __builtin_amdgcn_mfma_f32_32x32x16_bf16(b1, qr[d0], d0 == 0 ? negm : p1, 0, 0, 0); }
; }
; template <int D0> DI void pv_one(f32x16& od, int vb, bf16x8 pa0, bf16x8 pa1, bf16x8 pa2, bf16x8 pa3) {
;     const s16x4 l0 = tr_read<v_rd_off(D0, 0, 0)>(vb), h0 = tr_read<v_rd_off(D0, 0, 1)>(vb), l1 = tr_read<v_rd_off(D0, 1, 0)>(vb), h1 = tr_read<v_rd_off(D0, 1, 1)>(vb);
;     const s16x4 l2 = tr_read<v_rd_off(D0, 2, 0)>(vb), h2 = tr_read<v_rd_off(D0, 2, 1)>(vb), l3 = tr_read<v_rd_off(D0, 3, 0)>(vb), h3 = tr_read<v_rd_off(D0, 3, 1)>(vb);
;     asm volatile("s_waitcnt lgkmcnt(0)" ::: "memory"); AT_SBAR();
;     ...
;     od = __builtin_amdgcn_mfma_f32_32x32x16_bf16(AT_PK(l0, h0), pa0, od, 0, 0, 0);
;     od = __builtin_amdgcn_mfma_f32_32x32x16_bf16(AT_PK(l1, h1), pa1, od, 0, 0, 0);
;     od = __builtin_amdgcn_mfma_f32_32x32x16_bf16(AT_PK(l2, h2), pa2, od, 0, 0, 0);
;     od = __builtin_amdgcn_mfma_f32_32x32x16_bf16(AT_PK(l3, h3), pa3, od, 0, 0, 0);
;     ...
; }
.LBB4_923:
	s_lshl_b32 s18, s30, 13
	s_add_i32 s18, s18, 0
	v_add_u32_e32 v72, s18, v208
	v_add_u32_e32 v112, s18, v209
	v_add_u32_e32 v180, s18, v210
	s_waitcnt lgkmcnt(1)
	v_mfma_f32_32x32x16_bf16 v[128:143], v[64:67], v[156:159], v[80:95]
	ds_read_b128 v[64:67], v72 offset:49152
	ds_read_b128 v[72:75], v72 offset:53248
	ds_read_b128 v[76:79], v112 offset:49152
	ds_read_b128 v[224:227], v112 offset:53248
	s_add_u32 s34, s46, s16
	s_addc_u32 s35, s47, s17
	s_add_u32 s24, s34, 0x23808000
	s_addc_u32 s25, s35, 0
	s_add_u32 s54, s34, 0x2380a000
	s_add_u32 s42, s46, s20
	s_addc_u32 s43, s47, s21
	s_add_u32 s56, s42, 0x21884000
	s_addc_u32 s57, s43, 0
	s_lshl_b32 s92, s15, 14
	s_add_i32 s92, s92, s94
	s_mov_b32 m0, s92
	s_lshl_b32 s96, s15, 13
	global_load_lds_dwordx4 v249, s[24:25]
	s_addk_i32 s92, 0x400
	s_mov_b32 m0, s92
	s_add_i32 s96, s96, s95
	global_load_lds_dwordx4 v250, s[24:25]
	s_nop 0
	s_mov_b32 m0, s96
	s_nop 0
	global_load_lds_dwordx4 v251, s[56:57]
	v_exp_f32_e32 v182, v97
	v_exp_f32_e32 v217, v98
	v_exp_f32_e32 v218, v99
	v_exp_f32_e32 v223, v100
	v_exp_f32_e32 v232, v101
	s_waitcnt lgkmcnt(4)
	v_mfma_f32_32x32x16_bf16 v[112:127], v[68:71], v[156:159], v[80:95]
	ds_read_b128 v[68:71], v180 offset:49152
	ds_read_b128 v[228:231], v180 offset:53248
	v_exp_f32_e32 v180, v96
	v_cvt_pk_bf16_f32 v96, v220, v222
	v_cvt_pk_bf16_f32 v97, v179, v221
	v_cvt_pk_bf16_f32 v98, v177, v219
	v_cvt_pk_bf16_f32 v99, v176, v178
	s_waitcnt lgkmcnt(4)
	v_mfma_f32_32x32x16_bf16 v[112:127], v[72:75], v[152:155], v[112:127]
	v_add_f32_e32 v75, 0, v220
	v_add_f32_e32 v75, v222, v75
	v_add_f32_e32 v75, v179, v75
	v_add_f32_e32 v75, v221, v75
	v_add_f32_e32 v75, v177, v75
	v_add_f32_e32 v75, v219, v75
	v_add_f32_e32 v75, v176, v75
	v_mfma_f32_32x32x16_bf16 v[128:143], v[64:67], v[152:155], v[128:143]
	v_add_f32_e32 v75, v178, v75
	v_add_f32_e32 v75, v173, v75
	v_add_f32_e32 v75, v175, v75
	v_add_f32_e32 v75, v171, v75
	v_add_f32_e32 v75, v174, v75
	v_add_f32_e32 v75, v169, v75
	v_add_f32_e32 v75, v172, v75
	s_waitcnt lgkmcnt(3)
	v_mfma_f32_32x32x16_bf16 v[128:143], v[76:79], v[148:151], v[128:143]
	v_add_f32_e32 v75, v168, v75
	v_add_f32_e32 v75, v170, v75
	v_add_f32_e32 v75, v180, v75
	v_add_f32_e32 v75, v182, v75
	v_exp_f32_e32 v64, v102
	v_exp_f32_e32 v65, v103
	v_exp_f32_e32 v66, v104
	s_waitcnt lgkmcnt(2)
	v_mfma_f32_32x32x16_bf16 v[112:127], v[224:227], v[148:151], v[112:127]
	v_exp_f32_e32 v67, v105
	v_exp_f32_e32 v105, v106
	v_exp_f32_e32 v106, v107
	v_exp_f32_e32 v107, v108
	v_exp_f32_e32 v72, v109
	v_exp_f32_e32 v73, v110
	v_exp_f32_e32 v74, v111
	s_waitcnt lgkmcnt(1)
	v_mfma_f32_32x32x16_bf16 v[128:143], v[68:71], v[144:147], v[128:143]
	v_add_f32_e32 v68, v217, v75
	v_add_f32_e32 v68, v218, v68
	v_add_f32_e32 v68, v223, v68
	v_add_f32_e32 v68, v232, v68
	v_add_f32_e32 v68, v64, v68
	v_add_f32_e32 v68, v65, v68
	v_add_f32_e32 v68, v66, v68
	v_add_f32_e32 v68, v67, v68
	s_waitcnt lgkmcnt(0)
	v_mfma_f32_32x32x16_bf16 v[112:127], v[228:231], v[144:147], v[112:127]
	v_cvt_pk_bf16_f32 v100, v180, v182
	v_cvt_pk_bf16_f32 v103, v64, v65
	v_cvt_pk_bf16_f32 v104, v66, v67
	s_lshl_b32 s31, s29, 14
	v_add_u32_e32 v182, s31, v253
	ds_read_b64_tr_b16 v[64:65], v182 offset:0
	ds_read_b64_tr_b16 v[66:67], v182 offset:0x100
	v_add_f32_e32 v68, v105, v68
	v_add_f32_e32 v68, v106, v68
	v_add_f32_e32 v68, v107, v68
	v_add_f32_e32 v68, v72, v68
	v_add_f32_e32 v68, v73, v68
	v_add_f32_e32 v215, v74, v68
	ds_read_b64_tr_b16 v[68:69], v182 offset:0x1000
	ds_read_b64_tr_b16 v[70:71], v182 offset:0x1100
	v_cvt_pk_bf16_f32 v108, v173, v175
	v_cvt_pk_bf16_f32 v109, v171, v174
	v_cvt_pk_bf16_f32 v110, v169, v172
	v_cvt_pk_bf16_f32 v111, v168, v170
	v_cvt_pk_bf16_f32 v101, v217, v218
	v_cvt_pk_bf16_f32 v102, v223, v232
	v_cvt_pk_bf16_f32 v105, v105, v106
	v_cvt_pk_bf16_f32 v106, v107, v72
	v_cvt_pk_bf16_f32 v107, v73, v74
	s_nop 0
	s_waitcnt lgkmcnt(2)
	v_mfma_f32_32x32x16_bf16 v[48:63], v[64:67], v[96:99], v[48:63]
	s_addc_u32 s55, s35, 0
	s_andn2_b64 vcc, exec, s[2:3]
	s_cbranch_vccnz .LBB4_925
	s_mov_b64 s[2:3], s[8:9]
	global_store_dwordx2 v193, v[184:185], s[2:3] nt

; #define AT_SBAR() __builtin_amdgcn_sched_barrier(0)
; template <int OFF> DI s16x4 tr_read(int vb) { s16x4 r; asm volatile("ds_read_b64_tr_b16 %0, %1 offset:%2" : "=&v"(r) : "v"(vb), "i"(OFF) : "memory"); return r; }
; DI void finishSM(f32x16& p0, f32x16& p1, float alpha, float& l_reg, bf16x8& pa0, bf16x8& pa1, bf16x8& pa2, bf16x8& pa3) {
; #pragma unroll
;     for (int r = 0; r < 16; ++r) p1[r] = __builtin_amdgcn_exp2f(p1[r]);
;     float ps = 0;
; #pragma unroll
;     for (int r = 0; r < 16; ++r) ps += p0[r];
; #pragma unroll
;     for (int r = 0; r < 16; ++r) ps += p1[r];
;     { auto rr = __builtin_amdgcn_permlane32_swap(__float_as_uint(ps), __float_as_uint(ps), false, false); ps = __uint_as_float(rr[0]) + __uint_as_float(rr[1]); }
;     l_reg = l_reg * alpha + ps;
;     ...
;     AT_PK4(p0, 0, pa0); AT_PK4(p0, 8, pa1); AT_PK4(p1, 0, pa2); AT_PK4(p1, 8, pa3);
;     ...
; }
; DI void qkt(f32x16& p0, f32x16& p1, const char* Ks, const bf16x8* qr, const f32x16& negm, int r32, int hi) {
; #pragma unroll
;     for (int d0 = 0; d0 < 4; ++d0) { const int cb = (d0 * 16 + hi * 8) * 2;
;         const bf16x8 b0 = *reinterpret_cast<const bf16x8*>(Ks + AT_KSWZ(r32, cb));
;         const bf16x8 b1 = *reinterpret_cast<const bf16x8*>(Ks + AT_KSWZ(32 + r32, cb));
;         p0 = __builtin_amdgcn_mfma_f32_32x32x16_bf16(b0, qr[d0], d0 == 0 ? negm : p0, 0, 0, 0);
;         p1 = __builtin_amdgcn_mfma_f32_32x32x16_bf16(b1, qr[d0], d0 == 0 ? negm : p1, 0, 0, 0); }
; }
; template <int D0> DI void pv_one(f32x16& od, int vb, bf16x8 pa0, bf16x8 pa1, bf16x8 pa2, bf16x8 pa3) {
;     const s16x4 l0 = tr_read<v_rd_off(D0, 0, 0)>(vb), h0 = tr_read<v_rd_off(D0, 0, 1)>(vb), l1 = tr_read<v_rd_off(D0, 1, 0)>(vb), h1 = tr_read<v_rd_off(D0, 1, 1)>(vb);
;     const s16x4 l2 = tr_read<v_rd_off(D0, 2, 0)>(vb), h2 = tr_read<v_rd_off(D0, 2, 1)>(vb), l3 = tr_read<v_rd_off(D0, 3, 0)>(vb), h3 = tr_read<v_rd_off(D0, 3, 1)>(vb);
;     asm volatile("s_waitcnt lgkmcnt(0)" ::: "memory"); AT_SBAR();
;     ...
;     od = __builtin_amdgcn_mfma_f32_32x32x16_bf16(AT_PK(l0, h0), pa0, od, 0, 0, 0);
;     od = __builtin_amdgcn_mfma_f32_32x32x16_bf16(AT_PK(l1, h1), pa1, od, 0, 0, 0);
;     od = __builtin_amdgcn_mfma_f32_32x32x16_bf16(AT_PK(l2, h2), pa2, od, 0, 0, 0);
;     od = __builtin_amdgcn_mfma_f32_32x32x16_bf16(AT_PK(l3, h3), pa3, od, 0, 0, 0);
;     ...
; }
.LBB4_944:
	v_exp_f32_e32 v182, v128
	v_exp_f32_e32 v234, v129
	v_exp_f32_e32 v235, v130
	v_exp_f32_e32 v236, v131
	v_exp_f32_e32 v237, v132
	v_exp_f32_e32 v238, v133
	v_exp_f32_e32 v239, v134
	v_exp_f32_e32 v240, v135
	v_exp_f32_e32 v241, v136
	v_exp_f32_e32 v242, v137
	v_exp_f32_e32 v243, v138
	v_exp_f32_e32 v244, v139
	v_exp_f32_e32 v245, v140
	v_exp_f32_e32 v246, v141
	v_exp_f32_e32 v247, v142
	v_exp_f32_e32 v248, v143
	v_add_u32_e32 v101, s54, v208
	v_add_u32_e32 v102, s54, v209
	v_add_u32_e32 v103, s54, v210
	ds_read_b128 v[172:175], v101 offset:49152
	ds_read_b128 v[176:179], v101 offset:53248
	ds_read_b128 v[218:221], v102 offset:49152
	ds_read_b128 v[222:225], v102 offset:53248
	ds_read_b128 v[226:229], v103 offset:49152
	ds_read_b128 v[230:233], v103 offset:53248
	v_exp_f32_e32 v112, v112
	v_exp_f32_e32 v113, v113
	v_exp_f32_e32 v114, v114
	s_waitcnt lgkmcnt(7)
	v_mfma_f32_32x32x16_bf16 v[128:143], v[96:99], v[156:159], v[80:95]
	s_add_u32 s24, s34, 0x2380c000
	s_addc_u32 s25, s35, 0
	s_add_u32 s34, s34, 0x2380e000
	s_addc_u32 s35, s35, 0
	s_add_u32 s42, s42, 0x21886000
	s_addc_u32 s43, s43, 0
	s_lshl_b32 s92, s29, 14
	s_add_i32 s92, s92, s94
	s_mov_b32 m0, s92
	s_lshl_b32 s96, s29, 13
	global_load_lds_dwordx4 v249, s[24:25]
	s_addk_i32 s92, 0x400
	s_mov_b32 m0, s92
	s_add_i32 s96, s96, s95
	global_load_lds_dwordx4 v250, s[24:25]
	s_nop 0
	s_mov_b32 m0, s96
	s_nop 0
	global_load_lds_dwordx4 v251, s[42:43]
	s_nop 0
	v_exp_f32_e32 v115, v115
	v_exp_f32_e32 v116, v116
	v_exp_f32_e32 v117, v117
	v_exp_f32_e32 v118, v118
	v_exp_f32_e32 v119, v119
	s_waitcnt lgkmcnt(6)
	v_mfma_f32_32x32x16_bf16 v[96:111], v[168:171], v[156:159], v[80:95]
	v_exp_f32_e32 v168, v120
	v_add_f32_e32 v120, 0, v182
	v_add_f32_e32 v120, v234, v120
	v_add_f32_e32 v120, v235, v120
	v_add_f32_e32 v120, v236, v120
	v_add_f32_e32 v120, v237, v120
	v_add_f32_e32 v120, v238, v120
	v_add_f32_e32 v120, v239, v120
	v_add_f32_e32 v120, v240, v120
	v_add_f32_e32 v120, v241, v120
	v_add_f32_e32 v120, v242, v120
	s_waitcnt lgkmcnt(5)
	v_mfma_f32_32x32x16_bf16 v[128:143], v[172:175], v[152:155], v[128:143]
	v_add_f32_e32 v120, v243, v120
	v_add_f32_e32 v120, v244, v120
	v_add_f32_e32 v120, v245, v120
	v_add_f32_e32 v120, v246, v120
	v_add_f32_e32 v120, v247, v120
	v_add_f32_e32 v120, v248, v120
	v_add_f32_e32 v120, v112, v120
	s_waitcnt lgkmcnt(4)
	v_mfma_f32_32x32x16_bf16 v[96:111], v[176:179], v[152:155], v[96:111]
	v_add_f32_e32 v120, v113, v120
	v_add_f32_e32 v120, v114, v120
	v_add_f32_e32 v120, v115, v120
	v_add_f32_e32 v120, v116, v120
	v_exp_f32_e32 v169, v121
	v_add_f32_e32 v120, v117, v120
	v_exp_f32_e32 v170, v122
	s_waitcnt lgkmcnt(3)
	v_mfma_f32_32x32x16_bf16 v[128:143], v[218:221], v[148:151], v[128:143]
	v_add_f32_e32 v120, v118, v120
	v_exp_f32_e32 v171, v123
	v_add_f32_e32 v120, v119, v120
	v_exp_f32_e32 v172, v124
	v_add_f32_e32 v120, v168, v120
	v_exp_f32_e32 v173, v125
	v_add_f32_e32 v120, v169, v120
	s_waitcnt lgkmcnt(2)
	v_mfma_f32_32x32x16_bf16 v[96:111], v[222:225], v[148:151], v[96:111]
	v_exp_f32_e32 v174, v126
	v_add_f32_e32 v120, v170, v120
	v_exp_f32_e32 v175, v127
	v_add_f32_e32 v120, v171, v120
	v_add_f32_e32 v120, v172, v120
	v_add_f32_e32 v120, v173, v120
	v_add_f32_e32 v120, v174, v120
	s_waitcnt lgkmcnt(1)
	v_mfma_f32_32x32x16_bf16 v[128:143], v[226:229], v[144:147], v[128:143]
	v_add_f32_e32 v217, v175, v120
	v_cvt_pk_bf16_f32 v120, v182, v234
	v_cvt_pk_bf16_f32 v121, v235, v236
	v_cvt_pk_bf16_f32 v122, v237, v238
	v_cvt_pk_bf16_f32 v123, v239, v240
	v_cvt_pk_bf16_f32 v124, v241, v242
	s_waitcnt lgkmcnt(0)
	v_mfma_f32_32x32x16_bf16 v[96:111], v[230:233], v[144:147], v[96:111]
	v_lshl_add_u32 v219, s30, 14, v253
	ds_read_b64_tr_b16 v[220:221], v219 offset:0
	ds_read_b64_tr_b16 v[222:223], v219 offset:0x100
	ds_read_b64_tr_b16 v[224:225], v219 offset:0x1000
	ds_read_b64_tr_b16 v[226:227], v219 offset:0x1100
	v_cvt_pk_bf16_f32 v125, v243, v244
	v_cvt_pk_bf16_f32 v126, v245, v246
	v_cvt_pk_bf16_f32 v127, v247, v248
	v_cvt_pk_bf16_f32 v112, v112, v113
	v_cvt_pk_bf16_f32 v113, v114, v115
	v_cvt_pk_bf16_f32 v114, v116, v117
	v_cvt_pk_bf16_f32 v115, v118, v119
	v_cvt_pk_bf16_f32 v116, v168, v169
	v_cvt_pk_bf16_f32 v117, v170, v171
	v_cvt_pk_bf16_f32 v118, v172, v173
	v_cvt_pk_bf16_f32 v119, v174, v175
	s_nop 0
	s_waitcnt lgkmcnt(2)
	v_mfma_f32_32x32x16_bf16 v[48:63], v[220:223], v[120:123], v[48:63]
	s_and_b64 vcc, exec, s[2:3]
	s_cbranch_vccnz .LBB4_946
	s_mov_b64 s[2:3], s[8:9]
	global_store_dwordx2 v193, v[184:185], s[2:3] nt
